# staging loops unrolled with all loads in flight: silu(c) loop in mod, weight slab in norm1, router-weight staging (4 chunks) in norm2/route
# speedup vs baseline: 1.0177x; 1.0084x over previous
; __device__ __forceinline__ void phase_mod(const Ptrs& p, LAS unsigned char* lds) {
;     ...
;     for (int i = tid; i < B * D; i += 512) { const float v = p.c[i]; sc[i] = v / (1.0f + __expf(-v)); }
.LBB0_7:
	global_load_dword v20, v[2:3], off
	v_lshl_add_u64 v[2:3], v[2:3], 0, s[8:9]
	global_load_dword v21, v[2:3], off
	v_lshl_add_u64 v[2:3], v[2:3], 0, s[8:9]
	global_load_dword v22, v[2:3], off
	v_lshl_add_u64 v[2:3], v[2:3], 0, s[8:9]
	global_load_dword v23, v[2:3], off
	v_lshl_add_u64 v[2:3], v[2:3], 0, s[8:9]
	global_load_dword v24, v[2:3], off
	v_lshl_add_u64 v[2:3], v[2:3], 0, s[8:9]
	global_load_dword v25, v[2:3], off
	v_lshl_add_u64 v[2:3], v[2:3], 0, s[8:9]
	global_load_dword v26, v[2:3], off
	v_lshl_add_u64 v[2:3], v[2:3], 0, s[8:9]
	global_load_dword v27, v[2:3], off
	s_waitcnt vmcnt(0)
	v_mov_b32_e32 v7, v20
	v_mul_f32_e32 v8, 0xbfb8aa3b, v7
	v_exp_f32_e32 v8, v8
	s_nop 0
	v_add_f32_e32 v8, 1.0, v8
	v_div_scale_f32 v9, s[10:11], v8, v8, v7
	v_rcp_f32_e32 v10, v9
	v_div_scale_f32 v11, vcc, v7, v8, v7
	v_fma_f32 v12, -v9, v10, 1.0
	v_fmac_f32_e32 v10, v12, v10
	v_mul_f32_e32 v12, v11, v10
	v_fma_f32 v13, -v9, v12, v11
	v_fmac_f32_e32 v12, v13, v10
	v_fma_f32 v9, -v9, v12, v11
	v_div_fmas_f32 v9, v9, v10, v12
	v_div_fixup_f32 v7, v9, v8, v7
	ds_write_b32 v5, v7
	v_add_u32_e32 v5, 0x800, v5
	v_mov_b32_e32 v7, v21
	v_mul_f32_e32 v8, 0xbfb8aa3b, v7
	v_exp_f32_e32 v8, v8
	s_nop 0
	v_add_f32_e32 v8, 1.0, v8
	v_div_scale_f32 v9, s[10:11], v8, v8, v7
	v_rcp_f32_e32 v10, v9
	v_div_scale_f32 v11, vcc, v7, v8, v7
	v_fma_f32 v12, -v9, v10, 1.0
	v_fmac_f32_e32 v10, v12, v10
	v_mul_f32_e32 v12, v11, v10
	v_fma_f32 v13, -v9, v12, v11
	v_fmac_f32_e32 v12, v13, v10
	v_fma_f32 v9, -v9, v12, v11
	v_div_fmas_f32 v9, v9, v10, v12
	v_div_fixup_f32 v7, v9, v8, v7
	ds_write_b32 v5, v7
	v_add_u32_e32 v5, 0x800, v5
	v_mov_b32_e32 v7, v22
	v_mul_f32_e32 v8, 0xbfb8aa3b, v7
	v_exp_f32_e32 v8, v8
	s_nop 0
	v_add_f32_e32 v8, 1.0, v8
	v_div_scale_f32 v9, s[10:11], v8, v8, v7
	v_rcp_f32_e32 v10, v9
	v_div_scale_f32 v11, vcc, v7, v8, v7
	v_fma_f32 v12, -v9, v10, 1.0
	v_fmac_f32_e32 v10, v12, v10
	v_mul_f32_e32 v12, v11, v10
	v_fma_f32 v13, -v9, v12, v11
	v_fmac_f32_e32 v12, v13, v10
	v_fma_f32 v9, -v9, v12, v11
	v_div_fmas_f32 v9, v9, v10, v12
	v_div_fixup_f32 v7, v9, v8, v7
	ds_write_b32 v5, v7
	v_add_u32_e32 v5, 0x800, v5
	v_mov_b32_e32 v7, v23
	v_mul_f32_e32 v8, 0xbfb8aa3b, v7
	v_exp_f32_e32 v8, v8
	s_nop 0
	v_add_f32_e32 v8, 1.0, v8
	v_div_scale_f32 v9, s[10:11], v8, v8, v7
	v_rcp_f32_e32 v10, v9
	v_div_scale_f32 v11, vcc, v7, v8, v7
	v_fma_f32 v12, -v9, v10, 1.0
	v_fmac_f32_e32 v10, v12, v10
	v_mul_f32_e32 v12, v11, v10
	v_fma_f32 v13, -v9, v12, v11
	v_fmac_f32_e32 v12, v13, v10
	v_fma_f32 v9, -v9, v12, v11
	v_div_fmas_f32 v9, v9, v10, v12
	v_div_fixup_f32 v7, v9, v8, v7
	ds_write_b32 v5, v7
	v_add_u32_e32 v5, 0x800, v5
	v_mov_b32_e32 v7, v24
	v_mul_f32_e32 v8, 0xbfb8aa3b, v7
	v_exp_f32_e32 v8, v8
	s_nop 0
	v_add_f32_e32 v8, 1.0, v8
	v_div_scale_f32 v9, s[10:11], v8, v8, v7
	v_rcp_f32_e32 v10, v9
	v_div_scale_f32 v11, vcc, v7, v8, v7
	v_fma_f32 v12, -v9, v10, 1.0
	v_fmac_f32_e32 v10, v12, v10
	v_mul_f32_e32 v12, v11, v10
	v_fma_f32 v13, -v9, v12, v11
	v_fmac_f32_e32 v12, v13, v10
	v_fma_f32 v9, -v9, v12, v11
	v_div_fmas_f32 v9, v9, v10, v12
	v_div_fixup_f32 v7, v9, v8, v7
	ds_write_b32 v5, v7
	v_add_u32_e32 v5, 0x800, v5
	v_mov_b32_e32 v7, v25
	v_mul_f32_e32 v8, 0xbfb8aa3b, v7
	v_exp_f32_e32 v8, v8
	s_nop 0
	v_add_f32_e32 v8, 1.0, v8
	v_div_scale_f32 v9, s[10:11], v8, v8, v7
	v_rcp_f32_e32 v10, v9
	v_div_scale_f32 v11, vcc, v7, v8, v7
	v_fma_f32 v12, -v9, v10, 1.0
	v_fmac_f32_e32 v10, v12, v10
	v_mul_f32_e32 v12, v11, v10
	v_fma_f32 v13, -v9, v12, v11
	v_fmac_f32_e32 v12, v13, v10
	v_fma_f32 v9, -v9, v12, v11
	v_div_fmas_f32 v9, v9, v10, v12
	v_div_fixup_f32 v7, v9, v8, v7
	ds_write_b32 v5, v7
	v_add_u32_e32 v5, 0x800, v5
	v_mov_b32_e32 v7, v26
	v_mul_f32_e32 v8, 0xbfb8aa3b, v7
	v_exp_f32_e32 v8, v8
	s_nop 0
	v_add_f32_e32 v8, 1.0, v8
	v_div_scale_f32 v9, s[10:11], v8, v8, v7
	v_rcp_f32_e32 v10, v9
	v_div_scale_f32 v11, vcc, v7, v8, v7
	v_fma_f32 v12, -v9, v10, 1.0
	v_fmac_f32_e32 v10, v12, v10
	v_mul_f32_e32 v12, v11, v10
	v_fma_f32 v13, -v9, v12, v11
	v_fmac_f32_e32 v12, v13, v10
	v_fma_f32 v9, -v9, v12, v11
	v_div_fmas_f32 v9, v9, v10, v12
	v_div_fixup_f32 v7, v9, v8, v7
	ds_write_b32 v5, v7
	v_add_u32_e32 v5, 0x800, v5
	v_mov_b32_e32 v7, v27
	v_mul_f32_e32 v8, 0xbfb8aa3b, v7
	v_exp_f32_e32 v8, v8
	s_nop 0
	v_add_f32_e32 v8, 1.0, v8
	v_div_scale_f32 v9, s[10:11], v8, v8, v7
	v_rcp_f32_e32 v10, v9
	v_div_scale_f32 v11, vcc, v7, v8, v7
	v_fma_f32 v12, -v9, v10, 1.0
	v_fmac_f32_e32 v10, v12, v10
	v_mul_f32_e32 v12, v11, v10
	v_fma_f32 v13, -v9, v12, v11
	v_fmac_f32_e32 v12, v13, v10
	v_fma_f32 v9, -v9, v12, v11
	v_div_fmas_f32 v9, v9, v10, v12
	v_div_fixup_f32 v7, v9, v8, v7
	ds_write_b32 v5, v7

; #define LAS __attribute__((address_space(3)))
; __device__ __forceinline__ unsigned cvtpk(float lo, float hi) { f32x2_t v = {lo, hi}; bf16x2_t b = __builtin_convertvector(v, bf16x2_t); return __builtin_bit_cast(unsigned, b); }
; __device__ __forceinline__ void phase_norm1(const Ptrs& p, LAS unsigned char* lds) {
;     ...
;     for (int i = tid; i < 1024 * 4; i += 512) { const int kp = i >> 2, q = i & 3; const float* w = p.w_in + (size_t)(2 * kp) * NIN + W_F + q * 4;
;         const f32x4 v0 = *(const f32x4*)w, v1 = *(const f32x4*)(w + NIN);
; #pragma unroll
;         for (int j = 0; j < 4; ++j) *(LAS unsigned*)(lds + N1_WT + (q * 4 + j) * N1_PITCH + kp * 4) = cvtpk(v0[j], v1[j]); }
.LBB0_96:
	v_ashrrev_i32_e32 v4, 1, v7
	v_and_b32_e32 v11, 12, v6
	v_and_b32_e32 v8, -2, v4
	v_lshlrev_b32_e32 v4, 2, v11
	v_add_u32_e32 v20, 0, v8
	v_mad_i64_i32 v[12:13], s[6:7], v20, s2, v[2:3]
	v_lshl_add_u64 v[12:13], v[12:13], 0, v[4:5]
	v_add_co_u32_e32 v14, vcc, 0x6000, v12
	s_nop 1
	v_addc_co_u32_e32 v15, vcc, 0, v13, vcc
	v_add_co_u32_e32 v12, vcc, 0x10000, v12
	s_nop 1
	v_addc_co_u32_e32 v13, vcc, 0, v13, vcc
	global_load_dwordx4 v[120:123], v[14:15], off
	global_load_dwordx4 v[124:127], v[12:13], off offset:64
	v_add_u32_e32 v20, 256, v8
	v_mad_i64_i32 v[12:13], s[6:7], v20, s2, v[2:3]
	v_lshl_add_u64 v[12:13], v[12:13], 0, v[4:5]
	v_add_co_u32_e32 v14, vcc, 0x6000, v12
	s_nop 1
	v_addc_co_u32_e32 v15, vcc, 0, v13, vcc
	v_add_co_u32_e32 v12, vcc, 0x10000, v12
	s_nop 1
	v_addc_co_u32_e32 v13, vcc, 0, v13, vcc
	global_load_dwordx4 v[128:131], v[14:15], off
	global_load_dwordx4 v[132:135], v[12:13], off offset:64
	v_add_u32_e32 v20, 512, v8
	v_mad_i64_i32 v[12:13], s[6:7], v20, s2, v[2:3]
	v_lshl_add_u64 v[12:13], v[12:13], 0, v[4:5]
	v_add_co_u32_e32 v14, vcc, 0x6000, v12
	s_nop 1
	v_addc_co_u32_e32 v15, vcc, 0, v13, vcc
	v_add_co_u32_e32 v12, vcc, 0x10000, v12
	s_nop 1
	v_addc_co_u32_e32 v13, vcc, 0, v13, vcc
	global_load_dwordx4 v[136:139], v[14:15], off
	global_load_dwordx4 v[140:143], v[12:13], off offset:64
	v_add_u32_e32 v20, 768, v8
	v_mad_i64_i32 v[12:13], s[6:7], v20, s2, v[2:3]
	v_lshl_add_u64 v[12:13], v[12:13], 0, v[4:5]
	v_add_co_u32_e32 v14, vcc, 0x6000, v12
	s_nop 1
	v_addc_co_u32_e32 v15, vcc, 0, v13, vcc
	v_add_co_u32_e32 v12, vcc, 0x10000, v12
	s_nop 1
	v_addc_co_u32_e32 v13, vcc, 0, v13, vcc
	global_load_dwordx4 v[144:147], v[14:15], off
	global_load_dwordx4 v[148:151], v[12:13], off offset:64
	v_add_u32_e32 v20, 1024, v8
	v_mad_i64_i32 v[12:13], s[6:7], v20, s2, v[2:3]
	v_lshl_add_u64 v[12:13], v[12:13], 0, v[4:5]
	v_add_co_u32_e32 v14, vcc, 0x6000, v12
	s_nop 1
	v_addc_co_u32_e32 v15, vcc, 0, v13, vcc
	v_add_co_u32_e32 v12, vcc, 0x10000, v12
	s_nop 1
	v_addc_co_u32_e32 v13, vcc, 0, v13, vcc
	global_load_dwordx4 v[152:155], v[14:15], off
	global_load_dwordx4 v[156:159], v[12:13], off offset:64
	v_add_u32_e32 v20, 1280, v8
	v_mad_i64_i32 v[12:13], s[6:7], v20, s2, v[2:3]
	v_lshl_add_u64 v[12:13], v[12:13], 0, v[4:5]
	v_add_co_u32_e32 v14, vcc, 0x6000, v12
	s_nop 1
	v_addc_co_u32_e32 v15, vcc, 0, v13, vcc
	v_add_co_u32_e32 v12, vcc, 0x10000, v12
	s_nop 1
	v_addc_co_u32_e32 v13, vcc, 0, v13, vcc
	global_load_dwordx4 v[160:163], v[14:15], off
	global_load_dwordx4 v[164:167], v[12:13], off offset:64
	v_add_u32_e32 v20, 1536, v8
	v_mad_i64_i32 v[12:13], s[6:7], v20, s2, v[2:3]
	v_lshl_add_u64 v[12:13], v[12:13], 0, v[4:5]
	v_add_co_u32_e32 v14, vcc, 0x6000, v12
	s_nop 1
	v_addc_co_u32_e32 v15, vcc, 0, v13, vcc
	v_add_co_u32_e32 v12, vcc, 0x10000, v12
	s_nop 1
	v_addc_co_u32_e32 v13, vcc, 0, v13, vcc
	global_load_dwordx4 v[168:171], v[14:15], off
	global_load_dwordx4 v[172:175], v[12:13], off offset:64
	v_add_u32_e32 v20, 1792, v8
	v_mad_i64_i32 v[12:13], s[6:7], v20, s2, v[2:3]
	v_lshl_add_u64 v[12:13], v[12:13], 0, v[4:5]
	v_add_co_u32_e32 v14, vcc, 0x6000, v12
	s_nop 1
	v_addc_co_u32_e32 v15, vcc, 0, v13, vcc
	v_add_co_u32_e32 v12, vcc, 0x10000, v12
	s_nop 1
	v_addc_co_u32_e32 v13, vcc, 0, v13, vcc
	global_load_dwordx4 v[176:179], v[14:15], off
	global_load_dwordx4 v[180:183], v[12:13], off offset:64
	v_and_b32_e32 v4, -4, v7
	v_mul_u32_u24_e32 v9, 0x1010, v11
	v_add3_u32 v4, 0, v4, v9
	s_waitcnt vmcnt(0)
	v_cvt_pk_bf16_f32 v16, v120, v124
	v_cvt_pk_bf16_f32 v17, v121, v125
	v_cvt_pk_bf16_f32 v18, v122, v126
	v_cvt_pk_bf16_f32 v19, v123, v127
	ds_write_b32 v4, v16
	ds_write_b32 v4, v17 offset:4112
	ds_write_b32 v4, v18 offset:8224
	ds_write_b32 v4, v19 offset:12336
	v_cvt_pk_bf16_f32 v16, v128, v132
	v_cvt_pk_bf16_f32 v17, v129, v133
	v_cvt_pk_bf16_f32 v18, v130, v134
	v_cvt_pk_bf16_f32 v19, v131, v135
	ds_write_b32 v4, v16 offset:512
	ds_write_b32 v4, v17 offset:4624
	ds_write_b32 v4, v18 offset:8736
	ds_write_b32 v4, v19 offset:12848
	v_cvt_pk_bf16_f32 v16, v136, v140
	v_cvt_pk_bf16_f32 v17, v137, v141
	v_cvt_pk_bf16_f32 v18, v138, v142
	v_cvt_pk_bf16_f32 v19, v139, v143
	ds_write_b32 v4, v16 offset:1024
	ds_write_b32 v4, v17 offset:5136
	ds_write_b32 v4, v18 offset:9248
	ds_write_b32 v4, v19 offset:13360
	v_cvt_pk_bf16_f32 v16, v144, v148
	v_cvt_pk_bf16_f32 v17, v145, v149
	v_cvt_pk_bf16_f32 v18, v146, v150
	v_cvt_pk_bf16_f32 v19, v147, v151
	ds_write_b32 v4, v16 offset:1536
	ds_write_b32 v4, v17 offset:5648
	ds_write_b32 v4, v18 offset:9760
	ds_write_b32 v4, v19 offset:13872
	v_cvt_pk_bf16_f32 v16, v152, v156
	v_cvt_pk_bf16_f32 v17, v153, v157
	v_cvt_pk_bf16_f32 v18, v154, v158
	v_cvt_pk_bf16_f32 v19, v155, v159
	ds_write_b32 v4, v16 offset:2048
	ds_write_b32 v4, v17 offset:6160
	ds_write_b32 v4, v18 offset:10272
	ds_write_b32 v4, v19 offset:14384
	v_cvt_pk_bf16_f32 v16, v160, v164
	v_cvt_pk_bf16_f32 v17, v161, v165
	v_cvt_pk_bf16_f32 v18, v162, v166
	v_cvt_pk_bf16_f32 v19, v163, v167
	ds_write_b32 v4, v16 offset:2560
	ds_write_b32 v4, v17 offset:6672
	ds_write_b32 v4, v18 offset:10784
	ds_write_b32 v4, v19 offset:14896
	v_cvt_pk_bf16_f32 v16, v168, v172
	v_cvt_pk_bf16_f32 v17, v169, v173
	v_cvt_pk_bf16_f32 v18, v170, v174
	v_cvt_pk_bf16_f32 v19, v171, v175
	ds_write_b32 v4, v16 offset:3072
	ds_write_b32 v4, v17 offset:7184
	ds_write_b32 v4, v18 offset:11296
	ds_write_b32 v4, v19 offset:15408
	v_cvt_pk_bf16_f32 v16, v176, v180
	v_cvt_pk_bf16_f32 v17, v177, v181
	v_cvt_pk_bf16_f32 v18, v178, v182
	v_cvt_pk_bf16_f32 v19, v179, v183
	ds_write_b32 v4, v16 offset:3584
	ds_write_b32 v4, v17 offset:7696
	ds_write_b32 v4, v18 offset:11808
	ds_write_b32 v4, v19 offset:15920

; #define LAS __attribute__((address_space(3)))
; __device__ __forceinline__ unsigned cvtpk(float lo, float hi) { f32x2_t v = {lo, hi}; bf16x2_t b = __builtin_convertvector(v, bf16x2_t); return __builtin_bit_cast(unsigned, b); }
; __device__ __forceinline__ float wave_sum(float v) { v += dppf<DPP_XOR1>(v); v += dppf<DPP_XOR2>(v); v += dppf<DPP_XOR7>(v); v += dppf<DPP_XOR8>(v); return xrow_sum(v); }
; __device__ __forceinline__ void phase_norm2_route(const Ptrs& p, LAS unsigned char* lds) {
;     ...
;             for (int q = 0; q < 2; ++q) { const int row = blk * 32 + half * 16 + wid * 2 + q; const float* xr = x1 + (size_t)row * D; float ss = 0.f;
; #pragma unroll
;                 for (int c = 0; c < 8; ++c) { v[q][c] = __builtin_nontemporal_load((const f32x4*)(xr + c * 256 + lane * 4)); ss += v[q][c][0] * v[q][c][0] + v[q][c][1] * v[q][c][1] + v[q][c][2] * v[q][c][2] + v[q][c][3] * v[q][c][3]; }
;                 ss = wave_sum(ss); const float r = rsqrtf(ss * (1.0f / D) + EPS);
; #pragma unroll
;                 for (int c = 0; c < 8; ++c) { const int k = c * 256 + lane * 4; const f32x4 g4 = *(const LAS f32x4*)(gs + k), s4 = *(const LAS f32x4*)(sh + k);
;                     v[q][c] = (v[q][c] * r) * g4 + s4; u32x2 w; w.x = cvtpk(v[q][c][0], v[q][c][1]); w.y = cvtpk(v[q][c][2], v[q][c][3]); *(u32x2*)(ha + (size_t)row * D + k) = w; } }
.LBB0_925:
	v_lshl_add_u32 v120, s28, 4, v83
	v_ashrrev_i32_e32 v121, 31, v120
	v_lshlrev_b64 v[2:3], 13, v[120:121]
	v_lshl_add_u64 v[2:3], v[74:75], 0, v[2:3]
	global_load_dwordx4 v[42:45], v[2:3], off nt
	global_load_dwordx4 v[46:49], v[2:3], off offset:1024 nt
	global_load_dwordx4 v[50:53], v[2:3], off offset:2048 nt
	global_load_dwordx4 v[54:57], v[2:3], off offset:3072 nt
	v_add_co_u32_e32 v2, vcc, s64, v2
	v_lshlrev_b64 v[92:93], 12, v[120:121]
	s_nop 0
	v_addc_co_u32_e32 v3, vcc, 0, v3, vcc
	global_load_dwordx4 v[58:61], v[2:3], off nt
	global_load_dwordx4 v[62:65], v[2:3], off offset:1024 nt
	global_load_dwordx4 v[88:91], v[2:3], off offset:2048 nt
	global_load_dwordx4 v[66:69], v[2:3], off offset:3072 nt
	ds_read_b128 v[2:5], v158
	ds_read_b128 v[6:9], v159
	ds_read_b128 v[10:13], v160
	ds_read_b128 v[14:17], v161
	ds_read_b128 v[18:21], v162
	ds_read_b128 v[22:25], v163
	ds_read_b128 v[26:29], v164
	ds_read_b128 v[30:33], v165
	v_lshl_add_u64 v[122:123], v[86:87], 0, v[92:93]
	v_or_b32_e32 v124, 1, v120
	v_ashrrev_i32_e32 v125, 31, v124
	v_lshlrev_b64 v[120:121], 13, v[124:125]
	v_lshl_add_u64 v[134:135], v[74:75], 0, v[120:121]
	v_lshlrev_b64 v[124:125], 12, v[124:125]
	v_lshl_add_u64 v[208:209], v[86:87], 0, v[124:125]
	s_waitcnt vmcnt(7)
	v_mul_f32_e32 v34, v43, v43
	s_waitcnt vmcnt(6)
	v_mul_f32_e32 v35, v47, v47
	s_waitcnt vmcnt(5)
	v_mul_f32_e32 v36, v51, v51
	v_fmac_f32_e32 v34, v42, v42
	v_fmac_f32_e32 v35, v46, v46
	s_waitcnt vmcnt(4)
	v_mul_f32_e32 v37, v55, v55
	v_fmac_f32_e32 v36, v50, v50
	v_fmac_f32_e32 v34, v44, v44
	v_fmac_f32_e32 v35, v48, v48
	v_fmac_f32_e32 v37, v54, v54
	s_waitcnt vmcnt(3)
	v_mul_f32_e32 v38, v59, v59
	v_fmac_f32_e32 v36, v52, v52
	v_fmac_f32_e32 v34, v45, v45
	v_fmac_f32_e32 v35, v49, v49
	s_waitcnt vmcnt(2)
	v_mul_f32_e32 v39, v63, v63
	v_fmac_f32_e32 v37, v56, v56
	v_fmac_f32_e32 v38, v58, v58
	v_fmac_f32_e32 v36, v53, v53
	v_add_f32_e32 v34, v34, v35
	s_waitcnt vmcnt(1)
	v_mul_f32_e32 v40, v89, v89
	v_fmac_f32_e32 v39, v62, v62
	v_fmac_f32_e32 v37, v57, v57
	v_fmac_f32_e32 v38, v60, v60
	v_add_f32_e32 v34, v34, v36
	s_waitcnt vmcnt(0)
	v_mul_f32_e32 v41, v67, v67
	v_fmac_f32_e32 v40, v88, v88
	v_fmac_f32_e32 v39, v64, v64
	v_fmac_f32_e32 v38, v61, v61
	v_add_f32_e32 v34, v34, v37
	v_fmac_f32_e32 v41, v66, v66
	v_fmac_f32_e32 v40, v90, v90
	v_fmac_f32_e32 v39, v65, v65
	v_add_f32_e32 v34, v34, v38
	v_fmac_f32_e32 v41, v68, v68
	v_fmac_f32_e32 v40, v91, v91
	v_add_f32_e32 v34, v34, v39
	v_fmac_f32_e32 v41, v69, v69
	v_add_f32_e32 v34, v34, v40
	v_add_f32_e32 v34, v34, v41
	s_nop 1
	v_add_f32_dpp v34, v34, v34 quad_perm:[1,0,3,2] row_mask:0xf bank_mask:0xf bound_ctrl:1
	s_nop 1
	v_add_f32_dpp v34, v34, v34 quad_perm:[2,3,0,1] row_mask:0xf bank_mask:0xf bound_ctrl:1
	s_nop 1
	v_add_f32_dpp v34, v34, v34 row_half_mirror row_mask:0xf bank_mask:0xf bound_ctrl:1
	s_nop 1
	v_add_f32_dpp v34, v34, v34 row_ror:8 row_mask:0xf bank_mask:0xf bound_ctrl:1
	v_mov_b32_e32 v35, v34
	s_nop 1
	v_permlane16_swap_b32_e32 v34, v35
	v_add_f32_e32 v34, v34, v35
	v_mov_b32_e32 v35, v34
	s_nop 1
	v_permlane32_swap_b32_e32 v34, v35
	v_add_f32_e32 v34, v34, v35
	v_fmamk_f32 v34, v34, 0x3a000000, v179
	v_mul_f32_e32 v35, 0x4b800000, v34
	v_cmp_gt_f32_e32 vcc, s69, v34
	s_nop 1
	v_cndmask_b32_e32 v34, v34, v35, vcc
	v_rsq_f32_e32 v72, v34
	ds_read_b128 v[34:37], v166
	ds_read_b128 v[38:41], v167
	v_mul_f32_e32 v92, 0x45800000, v72
	v_cndmask_b32_e32 v72, v72, v92, vcc
	v_pk_mul_f32 v[42:43], v[42:43], v[72:73] op_sel_hi:[1,0]
	v_pk_mul_f32 v[44:45], v[44:45], v[72:73] op_sel_hi:[1,0]
	v_pk_mul_f32 v[46:47], v[46:47], v[72:73] op_sel_hi:[1,0]
	v_pk_mul_f32 v[48:49], v[48:49], v[72:73] op_sel_hi:[1,0]
	v_pk_mul_f32 v[50:51], v[50:51], v[72:73] op_sel_hi:[1,0]
	v_pk_mul_f32 v[52:53], v[52:53], v[72:73] op_sel_hi:[1,0]
	v_pk_mul_f32 v[54:55], v[54:55], v[72:73] op_sel_hi:[1,0]
	v_pk_mul_f32 v[56:57], v[56:57], v[72:73] op_sel_hi:[1,0]
	s_waitcnt lgkmcnt(8)
	v_pk_fma_f32 v[140:141], v[4:5], v[44:45], v[8:9]
	v_pk_fma_f32 v[142:143], v[2:3], v[42:43], v[6:7]
	s_waitcnt lgkmcnt(6)
	v_pk_fma_f32 v[126:127], v[12:13], v[48:49], v[16:17]
	v_pk_fma_f32 v[132:133], v[10:11], v[46:47], v[14:15]
	s_waitcnt lgkmcnt(4)
	v_pk_fma_f32 v[116:117], v[20:21], v[52:53], v[24:25]
	v_pk_fma_f32 v[118:119], v[18:19], v[50:51], v[22:23]
	s_waitcnt lgkmcnt(2)
	v_pk_fma_f32 v[108:109], v[28:29], v[56:57], v[32:33]
	v_pk_fma_f32 v[110:111], v[26:27], v[54:55], v[30:31]
	v_cvt_pk_bf16_f32 v136, v142, v143
	v_cvt_pk_bf16_f32 v137, v140, v141
	v_cvt_pk_bf16_f32 v138, v132, v133
	v_cvt_pk_bf16_f32 v139, v126, v127
	v_cvt_pk_bf16_f32 v112, v118, v119
	v_cvt_pk_bf16_f32 v113, v116, v117
	v_cvt_pk_bf16_f32 v114, v110, v111
	v_cvt_pk_bf16_f32 v115, v108, v109
	global_store_dwordx2 v[122:123], v[136:137], off
	global_store_dwordx2 v[122:123], v[138:139], off offset:512
	global_store_dwordx2 v[122:123], v[112:113], off offset:1024
	global_store_dwordx2 v[122:123], v[114:115], off offset:1536
	ds_read_b128 v[42:45], v168
	ds_read_b128 v[46:49], v169
	v_pk_mul_f32 v[58:59], v[58:59], v[72:73] op_sel_hi:[1,0]
	v_pk_mul_f32 v[60:61], v[60:61], v[72:73] op_sel_hi:[1,0]
	s_waitcnt lgkmcnt(2)
	v_pk_fma_f32 v[100:101], v[34:35], v[58:59], v[38:39]
	v_pk_fma_f32 v[98:99], v[36:37], v[60:61], v[40:41]
	v_cvt_pk_bf16_f32 v96, v100, v101
	v_cvt_pk_bf16_f32 v97, v98, v99
	global_store_dwordx2 v[122:123], v[96:97], off offset:2048
	v_pk_mul_f32 v[50:51], v[62:63], v[72:73] op_sel_hi:[1,0]
	v_pk_mul_f32 v[52:53], v[64:65], v[72:73] op_sel_hi:[1,0]
	s_waitcnt lgkmcnt(0)
; #define LAS __attribute__((address_space(3)))
; __device__ __forceinline__ unsigned cvtpk(float lo, float hi) { f32x2_t v = {lo, hi}; bf16x2_t b = __builtin_convertvector(v, bf16x2_t); return __builtin_bit_cast(unsigned, b); }
; __device__ __forceinline__ float wave_sum(float v) { v += dppf<DPP_XOR1>(v); v += dppf<DPP_XOR2>(v); v += dppf<DPP_XOR7>(v); v += dppf<DPP_XOR8>(v); return xrow_sum(v); }
; __device__ __forceinline__ void phase_norm2_route(const Ptrs& p, LAS unsigned char* lds) {
;     ...
;             for (int q = 0; q < 2; ++q) { const int row = blk * 32 + half * 16 + wid * 2 + q; const float* xr = x1 + (size_t)row * D; float ss = 0.f;
; #pragma unroll
;                 for (int c = 0; c < 8; ++c) { v[q][c] = __builtin_nontemporal_load((const f32x4*)(xr + c * 256 + lane * 4)); ss += v[q][c][0] * v[q][c][0] + v[q][c][1] * v[q][c][1] + v[q][c][2] * v[q][c][2] + v[q][c][3] * v[q][c][3]; }
;                 ss = wave_sum(ss); const float r = rsqrtf(ss * (1.0f / D) + EPS);
; #pragma unroll
;                 for (int c = 0; c < 8; ++c) { const int k = c * 256 + lane * 4; const f32x4 g4 = *(const LAS f32x4*)(gs + k), s4 = *(const LAS f32x4*)(sh + k);
;                     v[q][c] = (v[q][c] * r) * g4 + s4; u32x2 w; w.x = cvtpk(v[q][c][0], v[q][c][1]); w.y = cvtpk(v[q][c][2], v[q][c][3]); *(u32x2*)(ha + (size_t)row * D + k) = w; } }
	v_pk_fma_f32 v[106:107], v[50:51], v[42:43], v[46:47]
	v_pk_fma_f32 v[104:105], v[52:53], v[44:45], v[48:49]
	ds_read_b128 v[50:53], v170
	ds_read_b128 v[54:57], v171
	v_cvt_pk_bf16_f32 v102, v106, v107
	v_cvt_pk_bf16_f32 v103, v104, v105
	global_store_dwordx2 v[122:123], v[102:103], off offset:2560
	v_pk_mul_f32 v[58:59], v[88:89], v[72:73] op_sel_hi:[1,0]
	v_pk_mul_f32 v[60:61], v[90:91], v[72:73] op_sel_hi:[1,0]
	s_waitcnt lgkmcnt(0)
	v_pk_fma_f32 v[92:93], v[58:59], v[50:51], v[54:55]
	v_pk_fma_f32 v[90:91], v[60:61], v[52:53], v[56:57]
	ds_read_b128 v[58:61], v172
	ds_read_b128 v[62:65], v173
	v_pk_mul_f32 v[66:67], v[66:67], v[72:73] op_sel_hi:[1,0]
	v_pk_mul_f32 v[68:69], v[68:69], v[72:73] op_sel_hi:[1,0]
	v_cvt_pk_bf16_f32 v88, v92, v93
	v_cvt_pk_bf16_f32 v89, v90, v91
	s_waitcnt lgkmcnt(0)
	v_pk_fma_f32 v[68:69], v[68:69], v[60:61], v[64:65]
	v_pk_fma_f32 v[94:95], v[66:67], v[58:59], v[62:63]
	v_cvt_pk_bf16_f32 v67, v68, v69
	v_cvt_pk_bf16_f32 v66, v94, v95
	global_store_dwordx2 v[122:123], v[88:89], off offset:3072
	global_store_dwordx2 v[122:123], v[66:67], off offset:3584
	global_load_dwordx4 v[120:123], v[134:135], off nt
	s_nop 0
	global_load_dwordx4 v[128:131], v[134:135], off offset:1024 nt
	global_load_dwordx4 v[184:187], v[134:135], off offset:2048 nt
	global_load_dwordx4 v[188:191], v[134:135], off offset:3072 nt
	v_add_co_u32_e32 v134, vcc, s64, v134
	s_waitcnt vmcnt(3)
	v_mul_f32_e32 v72, v121, v121
	v_addc_co_u32_e32 v135, vcc, 0, v135, vcc
	global_load_dwordx4 v[192:195], v[134:135], off nt
	global_load_dwordx4 v[196:199], v[134:135], off offset:1024 nt
	global_load_dwordx4 v[200:203], v[134:135], off offset:2048 nt
	global_load_dwordx4 v[204:207], v[134:135], off offset:3072 nt
	s_waitcnt vmcnt(6)
	v_mul_f32_e32 v134, v129, v129
	s_waitcnt vmcnt(5)
	v_mul_f32_e32 v135, v185, v185
	v_fmac_f32_e32 v72, v120, v120
	v_fmac_f32_e32 v134, v128, v128
	s_waitcnt vmcnt(4)
	v_mul_f32_e32 v144, v189, v189
	v_fmac_f32_e32 v135, v184, v184
	v_fmac_f32_e32 v72, v122, v122
	v_fmac_f32_e32 v134, v130, v130
	v_fmac_f32_e32 v144, v188, v188
	v_fmac_f32_e32 v135, v186, v186
	v_fmac_f32_e32 v72, v123, v123
	v_fmac_f32_e32 v134, v131, v131
	v_fmac_f32_e32 v144, v190, v190
	v_fmac_f32_e32 v135, v187, v187
	v_add_f32_e32 v72, v72, v134
	v_fmac_f32_e32 v144, v191, v191
	v_add_f32_e32 v72, v72, v135
	v_add_f32_e32 v72, v72, v144
	s_waitcnt vmcnt(3)
	v_mul_f32_e32 v145, v193, v193
	s_waitcnt vmcnt(2)
	v_mul_f32_e32 v146, v197, v197
	v_fmac_f32_e32 v145, v192, v192
	s_waitcnt vmcnt(1)
	v_mul_f32_e32 v147, v201, v201
	v_fmac_f32_e32 v146, v196, v196
	v_fmac_f32_e32 v145, v194, v194
	s_waitcnt vmcnt(0)
	v_mul_f32_e32 v183, v205, v205
	v_fmac_f32_e32 v147, v200, v200
	v_fmac_f32_e32 v146, v198, v198
	v_fmac_f32_e32 v145, v195, v195
	v_fmac_f32_e32 v183, v204, v204
	v_fmac_f32_e32 v147, v202, v202
	v_fmac_f32_e32 v146, v199, v199
	v_add_f32_e32 v72, v72, v145
	v_fmac_f32_e32 v183, v206, v206
	v_fmac_f32_e32 v147, v203, v203
	v_add_f32_e32 v72, v72, v146
	v_fmac_f32_e32 v183, v207, v207
	v_add_f32_e32 v72, v72, v147
	v_add_f32_e32 v72, v72, v183
	s_nop 1
	v_add_f32_dpp v72, v72, v72 quad_perm:[1,0,3,2] row_mask:0xf bank_mask:0xf bound_ctrl:1
	s_nop 1
	v_add_f32_dpp v72, v72, v72 quad_perm:[2,3,0,1] row_mask:0xf bank_mask:0xf bound_ctrl:1
	s_nop 1
	v_add_f32_dpp v72, v72, v72 row_half_mirror row_mask:0xf bank_mask:0xf bound_ctrl:1
	s_nop 1
	v_add_f32_dpp v72, v72, v72 row_ror:8 row_mask:0xf bank_mask:0xf bound_ctrl:1
	v_mov_b32_e32 v134, v72
	s_nop 1
	v_permlane16_swap_b32_e32 v72, v134
	v_add_f32_e32 v72, v72, v134
	v_mov_b32_e32 v134, v72
	s_nop 1
	v_permlane32_swap_b32_e32 v72, v134
	v_add_f32_e32 v72, v72, v134
	v_fmamk_f32 v72, v72, 0x3a000000, v179
	v_mul_f32_e32 v134, 0x4b800000, v72
	v_cmp_gt_f32_e32 vcc, s69, v72
	s_nop 1
	v_cndmask_b32_e32 v72, v72, v134, vcc
	v_rsq_f32_e32 v72, v72
	s_nop 0
	v_mul_f32_e32 v124, 0x45800000, v72
	v_cndmask_b32_e32 v72, v72, v124, vcc
	v_pk_mul_f32 v[122:123], v[122:123], v[72:73] op_sel_hi:[1,0]
	v_pk_mul_f32 v[120:121], v[120:121], v[72:73] op_sel_hi:[1,0]
	v_pk_fma_f32 v[8:9], v[4:5], v[122:123], v[8:9]
	v_pk_mul_f32 v[4:5], v[130:131], v[72:73] op_sel_hi:[1,0]
	v_pk_mul_f32 v[124:125], v[128:129], v[72:73] op_sel_hi:[1,0]
	v_pk_fma_f32 v[146:147], v[2:3], v[120:121], v[6:7]
	v_pk_fma_f32 v[6:7], v[12:13], v[4:5], v[16:17]
	v_pk_mul_f32 v[12:13], v[186:187], v[72:73] op_sel_hi:[1,0]
	v_pk_fma_f32 v[144:145], v[10:11], v[124:125], v[14:15]
	v_pk_mul_f32 v[10:11], v[184:185], v[72:73] op_sel_hi:[1,0]
	v_pk_fma_f32 v[128:129], v[20:21], v[12:13], v[24:25]
	v_pk_mul_f32 v[12:13], v[190:191], v[72:73] op_sel_hi:[1,0]
	v_pk_fma_f32 v[134:135], v[18:19], v[10:11], v[22:23]
	v_pk_mul_f32 v[10:11], v[188:189], v[72:73] op_sel_hi:[1,0]
	v_pk_fma_f32 v[124:125], v[28:29], v[12:13], v[32:33]
	v_pk_mul_f32 v[12:13], v[194:195], v[72:73] op_sel_hi:[1,0]
	v_pk_fma_f32 v[130:131], v[26:27], v[10:11], v[30:31]
	v_pk_mul_f32 v[10:11], v[192:193], v[72:73] op_sel_hi:[1,0]
	v_pk_fma_f32 v[28:29], v[36:37], v[12:13], v[40:41]
	v_pk_mul_f32 v[12:13], v[198:199], v[72:73] op_sel_hi:[1,0]
	v_pk_fma_f32 v[32:33], v[34:35], v[10:11], v[38:39]
	v_pk_mul_f32 v[10:11], v[196:197], v[72:73] op_sel_hi:[1,0]
	v_pk_fma_f32 v[26:27], v[44:45], v[12:13], v[48:49]
	v_pk_mul_f32 v[12:13], v[202:203], v[72:73] op_sel_hi:[1,0]
	v_pk_fma_f32 v[30:31], v[42:43], v[10:11], v[46:47]
	v_pk_mul_f32 v[10:11], v[200:201], v[72:73] op_sel_hi:[1,0]
	v_pk_fma_f32 v[16:17], v[52:53], v[12:13], v[56:57]
	v_pk_mul_f32 v[12:13], v[204:205], v[72:73] op_sel_hi:[1,0]
	v_pk_mul_f32 v[14:15], v[206:207], v[72:73] op_sel_hi:[1,0]
	v_pk_fma_f32 v[20:21], v[50:51], v[10:11], v[54:55]
	v_pk_fma_f32 v[14:15], v[60:61], v[14:15], v[64:65]
	v_pk_fma_f32 v[18:19], v[58:59], v[12:13], v[62:63]
	v_cvt_pk_bf16_f32 v2, v146, v147
	v_cvt_pk_bf16_f32 v3, v8, v9
	v_cvt_pk_bf16_f32 v4, v144, v145
	v_cvt_pk_bf16_f32 v5, v6, v7
	v_cvt_pk_bf16_f32 v120, v134, v135
	v_cvt_pk_bf16_f32 v121, v128, v129
	v_cvt_pk_bf16_f32 v122, v130, v131
	v_cvt_pk_bf16_f32 v123, v124, v125
	v_cvt_pk_bf16_f32 v22, v32, v33
	v_cvt_pk_bf16_f32 v23, v28, v29
	v_cvt_pk_bf16_f32 v24, v30, v31
	v_cvt_pk_bf16_f32 v25, v26, v27
	v_cvt_pk_bf16_f32 v10, v20, v21
	v_cvt_pk_bf16_f32 v11, v16, v17
	v_cvt_pk_bf16_f32 v12, v18, v19
	v_cvt_pk_bf16_f32 v13, v14, v15
	global_store_dwordx2 v[208:209], v[2:3], off
	global_store_dwordx2 v[208:209], v[4:5], off offset:512
	global_store_dwordx2 v[208:209], v[120:121], off offset:1024
	global_store_dwordx2 v[208:209], v[122:123], off offset:1536
	global_store_dwordx2 v[208:209], v[22:23], off offset:2048
	global_store_dwordx2 v[208:209], v[24:25], off offset:2560
	global_store_dwordx2 v[208:209], v[10:11], off offset:3072
	global_store_dwordx2 v[208:209], v[12:13], off offset:3584
	s_barrier
; #define LAS __attribute__((address_space(3)))
; __device__ __forceinline__ unsigned cvtpk(float lo, float hi) { f32x2_t v = {lo, hi}; bf16x2_t b = __builtin_convertvector(v, bf16x2_t); return __builtin_bit_cast(unsigned, b); }
; __device__ __forceinline__ float bflo(unsigned w) { return __uint_as_float(w << 16); }
; __device__ __forceinline__ float bfhi(unsigned w) { return __uint_as_float(w & 0xffff0000u); }
; __device__ __forceinline__ void phase_norm2_route(const Ptrs& p, LAS unsigned char* lds) {
;     ...
;                 for (int i = tid; i < 2048; i += 512) { const int kp = i >> 3, cq = i & 7; const float* w = p.router_w + (size_t)(512 * ch + 2 * kp) * E + cq * 4;
;                     const f32x4 w0 = *(const f32x4*)w, w1 = *(const f32x4*)(w + E);
; #pragma unroll
;                     for (int j = 0; j < 4; ++j) { const unsigned hi = cvtpk(w0[j], w1[j]), lo = cvtpk(w0[j] - bflo(hi), w1[j] - bfhi(hi));
;                         *(LAS unsigned*)(lds + R_WHI + (cq * 4 + j) * R_PITCH + kp * 4) = hi; *(LAS unsigned*)(lds + R_WLO + (cq * 4 + j) * R_PITCH + kp * 4) = lo; } }
	s_and_saveexec_b64 s[46:47], s[4:5]
	s_cbranch_execz .LBB0_928
	v_mov_b32_e32 v34, v151
	v_mov_b32_e32 v35, v70
	v_ashrrev_i32_e32 v41, 3, v35
	v_lshlrev_b32_e32 v36, 1, v41
	v_ashrrev_i32_e32 v37, 31, v36
	v_and_b32_e32 v42, 28, v34
	v_lshlrev_b64 v[36:37], 7, v[36:37]
	v_lshlrev_b32_e32 v72, 2, v42
	v_lshl_add_u64 v[36:37], s[44:45], 0, v[36:37]
	v_lshl_add_u64 v[38:39], v[36:37], 0, v[72:73]
	v_lshlrev_b32_e32 v41, 2, v41
	v_mul_u32_u24_e32 v42, 0x410, v42
	v_add3_u32 v40, 0, v41, v42
	global_load_dwordx4 v[216:219], v[38:39], off
	global_load_dwordx4 v[220:223], v[38:39], off offset:128
	v_add_co_u32_e32 v36, vcc, 0x4000, v38
	s_nop 1
	v_addc_co_u32_e32 v37, vcc, 0, v39, vcc
	global_load_dwordx4 v[224:227], v[36:37], off
	global_load_dwordx4 v[228:231], v[36:37], off offset:128
	v_add_co_u32_e32 v36, vcc, 0x8000, v38
	s_nop 1
	v_addc_co_u32_e32 v37, vcc, 0, v39, vcc
	global_load_dwordx4 v[232:235], v[36:37], off
	global_load_dwordx4 v[236:239], v[36:37], off offset:128
	v_add_co_u32_e32 v36, vcc, 0xc000, v38
	s_nop 1
	v_addc_co_u32_e32 v37, vcc, 0, v39, vcc
	global_load_dwordx4 v[240:243], v[36:37], off
	global_load_dwordx4 v[248:251], v[36:37], off offset:128
	s_waitcnt vmcnt(0)
	v_cvt_pk_bf16_f32 v43, v216, v220
	v_cvt_pk_bf16_f32 v44, v217, v221
	v_cvt_pk_bf16_f32 v45, v218, v222
	v_cvt_pk_bf16_f32 v46, v219, v223
	ds_write_b32 v40, v43
	ds_write_b32 v40, v44 offset:1040
	ds_write_b32 v40, v45 offset:2080
	ds_write_b32 v40, v46 offset:3120
	v_lshlrev_b32_e32 v41, 16, v43
	v_and_b32_e32 v42, 0xffff0000, v43
	v_sub_f32_e32 v41, v216, v41
	v_sub_f32_e32 v42, v220, v42
	v_cvt_pk_bf16_f32 v43, v41, v42
	v_lshlrev_b32_e32 v41, 16, v44
	v_and_b32_e32 v42, 0xffff0000, v44
	v_sub_f32_e32 v41, v217, v41
	v_sub_f32_e32 v42, v221, v42
	v_cvt_pk_bf16_f32 v44, v41, v42
	v_lshlrev_b32_e32 v41, 16, v45
	v_and_b32_e32 v42, 0xffff0000, v45
	v_sub_f32_e32 v41, v218, v41
	v_sub_f32_e32 v42, v222, v42
	v_cvt_pk_bf16_f32 v45, v41, v42
	v_lshlrev_b32_e32 v41, 16, v46
	v_and_b32_e32 v42, 0xffff0000, v46
	v_sub_f32_e32 v41, v219, v41
	v_sub_f32_e32 v42, v223, v42
	v_cvt_pk_bf16_f32 v46, v41, v42
	ds_write_b32 v40, v43 offset:33280
	ds_write_b32 v40, v44 offset:34320
	ds_write_b32 v40, v45 offset:35360
	ds_write_b32 v40, v46 offset:36400
	v_cvt_pk_bf16_f32 v43, v224, v228
	v_cvt_pk_bf16_f32 v44, v225, v229
	v_cvt_pk_bf16_f32 v45, v226, v230
	v_cvt_pk_bf16_f32 v46, v227, v231
	ds_write_b32 v40, v43 offset:256
	ds_write_b32 v40, v44 offset:1296
	ds_write_b32 v40, v45 offset:2336
	ds_write_b32 v40, v46 offset:3376
	v_lshlrev_b32_e32 v41, 16, v43
	v_and_b32_e32 v42, 0xffff0000, v43
	v_sub_f32_e32 v41, v224, v41
	v_sub_f32_e32 v42, v228, v42
	v_cvt_pk_bf16_f32 v43, v41, v42
	v_lshlrev_b32_e32 v41, 16, v44
	v_and_b32_e32 v42, 0xffff0000, v44
	v_sub_f32_e32 v41, v225, v41
	v_sub_f32_e32 v42, v229, v42
	v_cvt_pk_bf16_f32 v44, v41, v42
	v_lshlrev_b32_e32 v41, 16, v45
	v_and_b32_e32 v42, 0xffff0000, v45
	v_sub_f32_e32 v41, v226, v41
	v_sub_f32_e32 v42, v230, v42
	v_cvt_pk_bf16_f32 v45, v41, v42
	v_lshlrev_b32_e32 v41, 16, v46
	v_and_b32_e32 v42, 0xffff0000, v46
	v_sub_f32_e32 v41, v227, v41
	v_sub_f32_e32 v42, v231, v42
	v_cvt_pk_bf16_f32 v46, v41, v42
	ds_write_b32 v40, v43 offset:33536
	ds_write_b32 v40, v44 offset:34576
	ds_write_b32 v40, v45 offset:35616
	ds_write_b32 v40, v46 offset:36656
	v_cvt_pk_bf16_f32 v43, v232, v236
	v_cvt_pk_bf16_f32 v44, v233, v237
	v_cvt_pk_bf16_f32 v45, v234, v238
	v_cvt_pk_bf16_f32 v46, v235, v239
	ds_write_b32 v40, v43 offset:512
	ds_write_b32 v40, v44 offset:1552
	ds_write_b32 v40, v45 offset:2592
	ds_write_b32 v40, v46 offset:3632
	v_lshlrev_b32_e32 v41, 16, v43
	v_and_b32_e32 v42, 0xffff0000, v43
	v_sub_f32_e32 v41, v232, v41
	v_sub_f32_e32 v42, v236, v42
	v_cvt_pk_bf16_f32 v43, v41, v42
	v_lshlrev_b32_e32 v41, 16, v44
	v_and_b32_e32 v42, 0xffff0000, v44
	v_sub_f32_e32 v41, v233, v41
	v_sub_f32_e32 v42, v237, v42
	v_cvt_pk_bf16_f32 v44, v41, v42
	v_lshlrev_b32_e32 v41, 16, v45
	v_and_b32_e32 v42, 0xffff0000, v45
	v_sub_f32_e32 v41, v234, v41
	v_sub_f32_e32 v42, v238, v42
	v_cvt_pk_bf16_f32 v45, v41, v42
	v_lshlrev_b32_e32 v41, 16, v46
	v_and_b32_e32 v42, 0xffff0000, v46
	v_sub_f32_e32 v41, v235, v41
	v_sub_f32_e32 v42, v239, v42
	v_cvt_pk_bf16_f32 v46, v41, v42
	ds_write_b32 v40, v43 offset:33792
	ds_write_b32 v40, v44 offset:34832
	ds_write_b32 v40, v45 offset:35872
	ds_write_b32 v40, v46 offset:36912
	v_cvt_pk_bf16_f32 v43, v240, v248
	v_cvt_pk_bf16_f32 v44, v241, v249
	v_cvt_pk_bf16_f32 v45, v242, v250
	v_cvt_pk_bf16_f32 v46, v243, v251
	ds_write_b32 v40, v43 offset:768
	ds_write_b32 v40, v44 offset:1808
	ds_write_b32 v40, v45 offset:2848
	ds_write_b32 v40, v46 offset:3888
	v_lshlrev_b32_e32 v41, 16, v43
	v_and_b32_e32 v42, 0xffff0000, v43
	v_sub_f32_e32 v41, v240, v41
	v_sub_f32_e32 v42, v248, v42
	v_cvt_pk_bf16_f32 v43, v41, v42
	v_lshlrev_b32_e32 v41, 16, v44
	v_and_b32_e32 v42, 0xffff0000, v44
	v_sub_f32_e32 v41, v241, v41
	v_sub_f32_e32 v42, v249, v42
	v_cvt_pk_bf16_f32 v44, v41, v42
	v_lshlrev_b32_e32 v41, 16, v45
	v_and_b32_e32 v42, 0xffff0000, v45
	v_sub_f32_e32 v41, v242, v41
	v_sub_f32_e32 v42, v250, v42
	v_cvt_pk_bf16_f32 v45, v41, v42
	v_lshlrev_b32_e32 v41, 16, v46
	v_and_b32_e32 v42, 0xffff0000, v46
	v_sub_f32_e32 v41, v243, v41
	v_sub_f32_e32 v42, v251, v42
	v_cvt_pk_bf16_f32 v46, v41, v42
	ds_write_b32 v40, v43 offset:34048
	ds_write_b32 v40, v44 offset:35088
	ds_write_b32 v40, v45 offset:36128
	ds_write_b32 v40, v46 offset:37168
; #define LAS __attribute__((address_space(3)))
; __device__ __forceinline__ unsigned cvtpk(float lo, float hi) { f32x2_t v = {lo, hi}; bf16x2_t b = __builtin_convertvector(v, bf16x2_t); return __builtin_bit_cast(unsigned, b); }
; __device__ __forceinline__ float bflo(unsigned w) { return __uint_as_float(w << 16); }
; __device__ __forceinline__ void phase_norm2_route(const Ptrs& p, LAS unsigned char* lds) {
;     ...
;                 for (int i = tid; i < 2048; i += 512) { const int kp = i >> 3, cq = i & 7; const float* w = p.router_w + (size_t)(512 * ch + 2 * kp) * E + cq * 4;
;                     const f32x4 w0 = *(const f32x4*)w, w1 = *(const f32x4*)(w + E);
; #pragma unroll
;                     for (int j = 0; j < 4; ++j) { const unsigned hi = cvtpk(w0[j], w1[j]), lo = cvtpk(w0[j] - bflo(hi), w1[j] - bfhi(hi));
;                         *(LAS unsigned*)(lds + R_WHI + (cq * 4 + j) * R_PITCH + kp * 4) = hi; *(LAS unsigned*)(lds + R_WLO + (cq * 4 + j) * R_PITCH + kp * 4) = lo; } }
; #pragma unroll
;                 for (int q = 0; q < 2; ++q)
; #pragma unroll
;                     for (int cc = 0; cc < 2; ++cc) { const f32x4 h4 = v[q][2 * ch + cc]; u32x2 hi, lo; hi.x = cvtpk(h4[0], h4[1]); hi.y = cvtpk(h4[2], h4[3]);
;                         lo.x = cvtpk(h4[0] - bflo(hi.x), h4[1] - bfhi(hi.x)); lo.y = cvtpk(h4[2] - bflo(hi.y), h4[3] - bfhi(hi.y));
;                         const int o = (wid * 2 + q) * R_PITCH + (cc * 256 + lane * 4) * 2;
;                         *(LAS u32x2*)(lds + R_HHI + o) = hi; *(LAS u32x2*)(lds + R_HLO + o) = lo; }
;                 __syncthreads();
; #pragma unroll
;                 for (int s2 = 0; s2 < 2; ++s2) { const int off = (lane & 15) * R_PITCH + (2 * wid + s2) * 64 + (lane >> 4) * 16;
;                     const bf16x8 ahi = *(const LAS bf16x8*)(lds + R_HHI + off), alo = *(const LAS bf16x8*)(lds + R_HLO + off);
; #pragma unroll
;                     for (int ct = 0; ct < 2; ++ct) { const bf16x8 bhi = *(const LAS bf16x8*)(lds + R_WHI + ct * 16 * R_PITCH + off), blo = *(const LAS bf16x8*)(lds + R_WLO + ct * 16 * R_PITCH + off);
;                         acc[ct] = __builtin_amdgcn_mfma_f32_16x16x32_bf16(ahi, bhi, acc[ct], 0, 0, 0); acc[ct] = __builtin_amdgcn_mfma_f32_16x16x32_bf16(alo, bhi, acc[ct], 0, 0, 0);
;                         acc[ct] = __builtin_amdgcn_mfma_f32_16x16x32_bf16(ahi, blo, acc[ct], 0, 0, 0); } }
.LBB0_928:
	s_or_b64 exec, exec, s[46:47]
	v_lshlrev_b32_e32 v34, 16, v136
	v_and_b32_e32 v35, 0xffff0000, v136
	v_pk_add_f32 v[34:35], v[142:143], v[34:35] neg_lo:[0,1] neg_hi:[0,1]
	v_lshlrev_b32_e32 v38, 16, v138
	v_cvt_pk_bf16_f32 v36, v34, v35
	v_lshlrev_b32_e32 v34, 16, v137
	v_and_b32_e32 v35, 0xffff0000, v137
	v_and_b32_e32 v39, 0xffff0000, v138
	v_lshlrev_b32_e32 v40, 16, v139
	v_and_b32_e32 v41, 0xffff0000, v139
	v_pk_add_f32 v[34:35], v[140:141], v[34:35] neg_lo:[0,1] neg_hi:[0,1]
	v_pk_add_f32 v[38:39], v[132:133], v[38:39] neg_lo:[0,1] neg_hi:[0,1]
	v_pk_add_f32 v[40:41], v[126:127], v[40:41] neg_lo:[0,1] neg_hi:[0,1]
	v_cvt_pk_bf16_f32 v37, v34, v35
	v_add_u32_e32 v34, s70, v78
	v_cvt_pk_bf16_f32 v38, v38, v39
	v_cvt_pk_bf16_f32 v39, v40, v41
	v_add_u32_e32 v35, s71, v78
	ds_write2st64_b64 v34, v[136:137], v[138:139] offset1:1
	ds_write2st64_b64 v35, v[36:37], v[38:39] offset1:1
	v_lshlrev_b32_e32 v36, 16, v2
	v_and_b32_e32 v37, 0xffff0000, v2
	v_lshlrev_b32_e32 v38, 16, v3
	v_and_b32_e32 v39, 0xffff0000, v3
	v_pk_add_f32 v[36:37], v[146:147], v[36:37] neg_lo:[0,1] neg_hi:[0,1]
	v_pk_add_f32 v[8:9], v[8:9], v[38:39] neg_lo:[0,1] neg_hi:[0,1]
	v_cvt_pk_bf16_f32 v36, v36, v37
	v_cvt_pk_bf16_f32 v37, v8, v9
	v_lshlrev_b32_e32 v8, 16, v4
	v_and_b32_e32 v9, 0xffff0000, v4
	v_lshlrev_b32_e32 v38, 16, v5
	v_and_b32_e32 v39, 0xffff0000, v5
	v_pk_add_f32 v[8:9], v[144:145], v[8:9] neg_lo:[0,1] neg_hi:[0,1]
	v_pk_add_f32 v[6:7], v[6:7], v[38:39] neg_lo:[0,1] neg_hi:[0,1]
	v_cvt_pk_bf16_f32 v8, v8, v9
	v_cvt_pk_bf16_f32 v9, v6, v7
	ds_write2_b64 v34, v[2:3], v[4:5] offset0:130 offset1:194
	ds_write2_b64 v35, v[36:37], v[8:9] offset0:130 offset1:194
	v_add_u32_e32 v37, s70, v150
	s_waitcnt lgkmcnt(0)
	s_barrier
	ds_read_b128 v[2:5], v37
	v_add_u32_e32 v36, 0, v150
	ds_read_b128 v[6:9], v36
	v_add_u32_e32 v38, s71, v150
	ds_read_b128 v[40:43], v37 offset:64
	ds_read_b128 v[44:47], v36 offset:64
	s_waitcnt lgkmcnt(2)
	v_mfma_f32_16x16x32_bf16 v[48:51], v[2:5], v[6:9], 0
	ds_read_b128 v[52:55], v38
	ds_read_b128 v[56:59], v38 offset:64
	s_xor_b64 s[46:47], s[54:55], -1
	s_waitcnt lgkmcnt(1)
	v_mfma_f32_16x16x32_bf16 v[6:9], v[52:55], v[6:9], v[48:51]
	s_nop 2
	ds_read_b128 v[48:51], v36 offset:33280
	ds_read_b128 v[60:63], v36 offset:33344
	s_waitcnt lgkmcnt(1)
	v_mfma_f32_16x16x32_bf16 v[6:9], v[2:5], v[48:51], v[6:9]
	ds_read_b128 v[48:51], v36 offset:16640
	ds_read_b128 v[136:139], v36 offset:16704
	s_waitcnt lgkmcnt(1)
	v_mfma_f32_16x16x32_bf16 v[140:143], v[2:5], v[48:51], 0
	v_mfma_f32_16x16x32_bf16 v[48:51], v[52:55], v[48:51], v[140:143]
	ds_read_b128 v[52:55], v36 offset:49920
	s_nop 5
	ds_read_b128 v[140:143], v36 offset:49984
	s_waitcnt lgkmcnt(0)
	s_barrier
	v_mfma_f32_16x16x32_bf16 v[2:5], v[2:5], v[52:55], v[48:51]
	v_mfma_f32_16x16x32_bf16 v[6:9], v[40:43], v[44:47], v[6:9]
	v_mfma_f32_16x16x32_bf16 v[2:5], v[40:43], v[136:139], v[2:5]
	v_mfma_f32_16x16x32_bf16 v[6:9], v[56:59], v[44:47], v[6:9]
	v_mfma_f32_16x16x32_bf16 v[2:5], v[56:59], v[136:139], v[2:5]
	v_mfma_f32_16x16x32_bf16 v[6:9], v[40:43], v[60:63], v[6:9]
	v_mfma_f32_16x16x32_bf16 v[2:5], v[40:43], v[140:143], v[2:5]
	s_and_saveexec_b64 s[54:55], s[4:5]
	s_cbranch_execz .LBB0_931
	v_mov_b32_e32 v39, v151
	v_mov_b32_e32 v40, v70
	v_ashrrev_i32_e32 v46, 3, v40
	v_lshlrev_b32_e32 v42, 1, v46
	v_ashrrev_i32_e32 v43, 31, v42
	v_and_b32_e32 v47, 28, v39
	v_lshlrev_b64 v[42:43], 7, v[42:43]
	v_lshlrev_b32_e32 v72, 2, v47
	v_lshl_add_u64 v[42:43], s[44:45], 0, v[42:43]
	v_lshl_add_u64 v[44:45], v[42:43], 0, v[72:73]
	v_lshlrev_b32_e32 v46, 2, v46
	v_mul_u32_u24_e32 v47, 0x410, v47
	v_add3_u32 v41, 0, v46, v47
	v_add_co_u32_e32 v42, vcc, 0x10000, v44
	s_nop 1
	v_addc_co_u32_e32 v43, vcc, 0, v45, vcc
	global_load_dwordx4 v[216:219], v[42:43], off
	global_load_dwordx4 v[220:223], v[42:43], off offset:128
	v_add_co_u32_e32 v42, vcc, 0x14000, v44
	s_nop 1
	v_addc_co_u32_e32 v43, vcc, 0, v45, vcc
	global_load_dwordx4 v[224:227], v[42:43], off
	global_load_dwordx4 v[228:231], v[42:43], off offset:128
	v_add_co_u32_e32 v42, vcc, 0x18000, v44
	s_nop 1
	v_addc_co_u32_e32 v43, vcc, 0, v45, vcc
	global_load_dwordx4 v[232:235], v[42:43], off
	global_load_dwordx4 v[236:239], v[42:43], off offset:128
	v_add_co_u32_e32 v42, vcc, 0x1c000, v44
	s_nop 1
	v_addc_co_u32_e32 v43, vcc, 0, v45, vcc
	global_load_dwordx4 v[240:243], v[42:43], off
	global_load_dwordx4 v[248:251], v[42:43], off offset:128
	s_waitcnt vmcnt(0)
; #define LAS __attribute__((address_space(3)))
; __device__ __forceinline__ unsigned cvtpk(float lo, float hi) { f32x2_t v = {lo, hi}; bf16x2_t b = __builtin_convertvector(v, bf16x2_t); return __builtin_bit_cast(unsigned, b); }
; __device__ __forceinline__ float bflo(unsigned w) { return __uint_as_float(w << 16); }
; __device__ __forceinline__ float bfhi(unsigned w) { return __uint_as_float(w & 0xffff0000u); }
; __device__ __forceinline__ void phase_norm2_route(const Ptrs& p, LAS unsigned char* lds) {
;     ...
;                 for (int i = tid; i < 2048; i += 512) { const int kp = i >> 3, cq = i & 7; const float* w = p.router_w + (size_t)(512 * ch + 2 * kp) * E + cq * 4;
;                     const f32x4 w0 = *(const f32x4*)w, w1 = *(const f32x4*)(w + E);
; #pragma unroll
;                     for (int j = 0; j < 4; ++j) { const unsigned hi = cvtpk(w0[j], w1[j]), lo = cvtpk(w0[j] - bflo(hi), w1[j] - bfhi(hi));
;                         *(LAS unsigned*)(lds + R_WHI + (cq * 4 + j) * R_PITCH + kp * 4) = hi; *(LAS unsigned*)(lds + R_WLO + (cq * 4 + j) * R_PITCH + kp * 4) = lo; } }
	v_cvt_pk_bf16_f32 v48, v216, v220
	v_cvt_pk_bf16_f32 v49, v217, v221
	v_cvt_pk_bf16_f32 v50, v218, v222
	v_cvt_pk_bf16_f32 v51, v219, v223
	ds_write_b32 v41, v48
	ds_write_b32 v41, v49 offset:1040
	ds_write_b32 v41, v50 offset:2080
	ds_write_b32 v41, v51 offset:3120
	v_lshlrev_b32_e32 v46, 16, v48
	v_and_b32_e32 v47, 0xffff0000, v48
	v_sub_f32_e32 v46, v216, v46
	v_sub_f32_e32 v47, v220, v47
	v_cvt_pk_bf16_f32 v48, v46, v47
	v_lshlrev_b32_e32 v46, 16, v49
	v_and_b32_e32 v47, 0xffff0000, v49
	v_sub_f32_e32 v46, v217, v46
	v_sub_f32_e32 v47, v221, v47
	v_cvt_pk_bf16_f32 v49, v46, v47
	v_lshlrev_b32_e32 v46, 16, v50
	v_and_b32_e32 v47, 0xffff0000, v50
	v_sub_f32_e32 v46, v218, v46
	v_sub_f32_e32 v47, v222, v47
	v_cvt_pk_bf16_f32 v50, v46, v47
	v_lshlrev_b32_e32 v46, 16, v51
	v_and_b32_e32 v47, 0xffff0000, v51
	v_sub_f32_e32 v46, v219, v46
	v_sub_f32_e32 v47, v223, v47
	v_cvt_pk_bf16_f32 v51, v46, v47
	ds_write_b32 v41, v48 offset:33280
	ds_write_b32 v41, v49 offset:34320
	ds_write_b32 v41, v50 offset:35360
	ds_write_b32 v41, v51 offset:36400
	v_cvt_pk_bf16_f32 v48, v224, v228
	v_cvt_pk_bf16_f32 v49, v225, v229
	v_cvt_pk_bf16_f32 v50, v226, v230
	v_cvt_pk_bf16_f32 v51, v227, v231
	ds_write_b32 v41, v48 offset:256
	ds_write_b32 v41, v49 offset:1296
	ds_write_b32 v41, v50 offset:2336
	ds_write_b32 v41, v51 offset:3376
	v_lshlrev_b32_e32 v46, 16, v48
	v_and_b32_e32 v47, 0xffff0000, v48
	v_sub_f32_e32 v46, v224, v46
	v_sub_f32_e32 v47, v228, v47
	v_cvt_pk_bf16_f32 v48, v46, v47
	v_lshlrev_b32_e32 v46, 16, v49
	v_and_b32_e32 v47, 0xffff0000, v49
	v_sub_f32_e32 v46, v225, v46
	v_sub_f32_e32 v47, v229, v47
	v_cvt_pk_bf16_f32 v49, v46, v47
	v_lshlrev_b32_e32 v46, 16, v50
	v_and_b32_e32 v47, 0xffff0000, v50
	v_sub_f32_e32 v46, v226, v46
	v_sub_f32_e32 v47, v230, v47
	v_cvt_pk_bf16_f32 v50, v46, v47
	v_lshlrev_b32_e32 v46, 16, v51
	v_and_b32_e32 v47, 0xffff0000, v51
	v_sub_f32_e32 v46, v227, v46
	v_sub_f32_e32 v47, v231, v47
	v_cvt_pk_bf16_f32 v51, v46, v47
	ds_write_b32 v41, v48 offset:33536
	ds_write_b32 v41, v49 offset:34576
	ds_write_b32 v41, v50 offset:35616
	ds_write_b32 v41, v51 offset:36656
	v_cvt_pk_bf16_f32 v48, v232, v236
	v_cvt_pk_bf16_f32 v49, v233, v237
	v_cvt_pk_bf16_f32 v50, v234, v238
	v_cvt_pk_bf16_f32 v51, v235, v239
	ds_write_b32 v41, v48 offset:512
	ds_write_b32 v41, v49 offset:1552
	ds_write_b32 v41, v50 offset:2592
	ds_write_b32 v41, v51 offset:3632
	v_lshlrev_b32_e32 v46, 16, v48
	v_and_b32_e32 v47, 0xffff0000, v48
	v_sub_f32_e32 v46, v232, v46
	v_sub_f32_e32 v47, v236, v47
	v_cvt_pk_bf16_f32 v48, v46, v47
	v_lshlrev_b32_e32 v46, 16, v49
	v_and_b32_e32 v47, 0xffff0000, v49
	v_sub_f32_e32 v46, v233, v46
	v_sub_f32_e32 v47, v237, v47
	v_cvt_pk_bf16_f32 v49, v46, v47
	v_lshlrev_b32_e32 v46, 16, v50
	v_and_b32_e32 v47, 0xffff0000, v50
	v_sub_f32_e32 v46, v234, v46
	v_sub_f32_e32 v47, v238, v47
	v_cvt_pk_bf16_f32 v50, v46, v47
	v_lshlrev_b32_e32 v46, 16, v51
	v_and_b32_e32 v47, 0xffff0000, v51
	v_sub_f32_e32 v46, v235, v46
	v_sub_f32_e32 v47, v239, v47
	v_cvt_pk_bf16_f32 v51, v46, v47
	ds_write_b32 v41, v48 offset:33792
	ds_write_b32 v41, v49 offset:34832
	ds_write_b32 v41, v50 offset:35872
	ds_write_b32 v41, v51 offset:36912
	v_cvt_pk_bf16_f32 v48, v240, v248
	v_cvt_pk_bf16_f32 v49, v241, v249
	v_cvt_pk_bf16_f32 v50, v242, v250
	v_cvt_pk_bf16_f32 v51, v243, v251
	ds_write_b32 v41, v48 offset:768
	ds_write_b32 v41, v49 offset:1808
	ds_write_b32 v41, v50 offset:2848
	ds_write_b32 v41, v51 offset:3888
	v_lshlrev_b32_e32 v46, 16, v48
	v_and_b32_e32 v47, 0xffff0000, v48
	v_sub_f32_e32 v46, v240, v46
	v_sub_f32_e32 v47, v248, v47
	v_cvt_pk_bf16_f32 v48, v46, v47
	v_lshlrev_b32_e32 v46, 16, v49
	v_and_b32_e32 v47, 0xffff0000, v49
	v_sub_f32_e32 v46, v241, v46
	v_sub_f32_e32 v47, v249, v47
	v_cvt_pk_bf16_f32 v49, v46, v47
	v_lshlrev_b32_e32 v46, 16, v50
	v_and_b32_e32 v47, 0xffff0000, v50
	v_sub_f32_e32 v46, v242, v46
	v_sub_f32_e32 v47, v250, v47
	v_cvt_pk_bf16_f32 v50, v46, v47
	v_lshlrev_b32_e32 v46, 16, v51
	v_and_b32_e32 v47, 0xffff0000, v51
	v_sub_f32_e32 v46, v243, v46
	v_sub_f32_e32 v47, v251, v47
	v_cvt_pk_bf16_f32 v51, v46, v47
	ds_write_b32 v41, v48 offset:34048
	ds_write_b32 v41, v49 offset:35088
	ds_write_b32 v41, v50 offset:36128
	ds_write_b32 v41, v51 offset:37168
; #define LAS __attribute__((address_space(3)))
; __device__ __forceinline__ unsigned cvtpk(float lo, float hi) { f32x2_t v = {lo, hi}; bf16x2_t b = __builtin_convertvector(v, bf16x2_t); return __builtin_bit_cast(unsigned, b); }
; __device__ __forceinline__ float bflo(unsigned w) { return __uint_as_float(w << 16); }
; __device__ __forceinline__ void phase_norm2_route(const Ptrs& p, LAS unsigned char* lds) {
;     ...
;                 for (int i = tid; i < 2048; i += 512) { const int kp = i >> 3, cq = i & 7; const float* w = p.router_w + (size_t)(512 * ch + 2 * kp) * E + cq * 4;
;                     const f32x4 w0 = *(const f32x4*)w, w1 = *(const f32x4*)(w + E);
; #pragma unroll
;                     for (int j = 0; j < 4; ++j) { const unsigned hi = cvtpk(w0[j], w1[j]), lo = cvtpk(w0[j] - bflo(hi), w1[j] - bfhi(hi));
;                         *(LAS unsigned*)(lds + R_WHI + (cq * 4 + j) * R_PITCH + kp * 4) = hi; *(LAS unsigned*)(lds + R_WLO + (cq * 4 + j) * R_PITCH + kp * 4) = lo; } }
; #pragma unroll
;                 for (int q = 0; q < 2; ++q)
; #pragma unroll
;                     for (int cc = 0; cc < 2; ++cc) { const f32x4 h4 = v[q][2 * ch + cc]; u32x2 hi, lo; hi.x = cvtpk(h4[0], h4[1]); hi.y = cvtpk(h4[2], h4[3]);
;                         lo.x = cvtpk(h4[0] - bflo(hi.x), h4[1] - bfhi(hi.x)); lo.y = cvtpk(h4[2] - bflo(hi.y), h4[3] - bfhi(hi.y));
;                         const int o = (wid * 2 + q) * R_PITCH + (cc * 256 + lane * 4) * 2;
;                         *(LAS u32x2*)(lds + R_HHI + o) = hi; *(LAS u32x2*)(lds + R_HLO + o) = lo; }
;                 __syncthreads();
; #pragma unroll
;                 for (int s2 = 0; s2 < 2; ++s2) { const int off = (lane & 15) * R_PITCH + (2 * wid + s2) * 64 + (lane >> 4) * 16;
;                     const bf16x8 ahi = *(const LAS bf16x8*)(lds + R_HHI + off), alo = *(const LAS bf16x8*)(lds + R_HLO + off);
; #pragma unroll
;                     for (int ct = 0; ct < 2; ++ct) { const bf16x8 bhi = *(const LAS bf16x8*)(lds + R_WHI + ct * 16 * R_PITCH + off), blo = *(const LAS bf16x8*)(lds + R_WLO + ct * 16 * R_PITCH + off);
;                         acc[ct] = __builtin_amdgcn_mfma_f32_16x16x32_bf16(ahi, bhi, acc[ct], 0, 0, 0); acc[ct] = __builtin_amdgcn_mfma_f32_16x16x32_bf16(alo, bhi, acc[ct], 0, 0, 0);
;                         acc[ct] = __builtin_amdgcn_mfma_f32_16x16x32_bf16(ahi, blo, acc[ct], 0, 0, 0); } }
.LBB0_931:
	s_or_b64 exec, exec, s[54:55]
	v_lshlrev_b32_e32 v40, 16, v112
	v_and_b32_e32 v41, 0xffff0000, v112
	v_lshlrev_b32_e32 v42, 16, v113
	v_and_b32_e32 v43, 0xffff0000, v113
	v_pk_add_f32 v[40:41], v[118:119], v[40:41] neg_lo:[0,1] neg_hi:[0,1]
	v_pk_add_f32 v[42:43], v[116:117], v[42:43] neg_lo:[0,1] neg_hi:[0,1]
	v_cvt_pk_bf16_f32 v40, v40, v41
	v_cvt_pk_bf16_f32 v41, v42, v43
	v_lshlrev_b32_e32 v42, 16, v114
	v_and_b32_e32 v43, 0xffff0000, v114
	v_lshlrev_b32_e32 v44, 16, v115
	v_and_b32_e32 v45, 0xffff0000, v115
	v_pk_add_f32 v[42:43], v[110:111], v[42:43] neg_lo:[0,1] neg_hi:[0,1]
	v_pk_add_f32 v[44:45], v[108:109], v[44:45] neg_lo:[0,1] neg_hi:[0,1]
	v_cvt_pk_bf16_f32 v42, v42, v43
	v_cvt_pk_bf16_f32 v43, v44, v45
	ds_write2st64_b64 v34, v[112:113], v[114:115] offset1:1
	ds_write2st64_b64 v35, v[40:41], v[42:43] offset1:1
	v_lshlrev_b32_e32 v40, 16, v120
	v_and_b32_e32 v41, 0xffff0000, v120
	v_lshlrev_b32_e32 v42, 16, v121
	v_and_b32_e32 v43, 0xffff0000, v121
	v_pk_add_f32 v[40:41], v[134:135], v[40:41] neg_lo:[0,1] neg_hi:[0,1]
	v_pk_add_f32 v[42:43], v[128:129], v[42:43] neg_lo:[0,1] neg_hi:[0,1]
	v_cvt_pk_bf16_f32 v40, v40, v41
	v_cvt_pk_bf16_f32 v41, v42, v43
	v_lshlrev_b32_e32 v42, 16, v122
	v_and_b32_e32 v43, 0xffff0000, v122
	v_lshlrev_b32_e32 v44, 16, v123
	v_and_b32_e32 v45, 0xffff0000, v123
	v_pk_add_f32 v[42:43], v[130:131], v[42:43] neg_lo:[0,1] neg_hi:[0,1]
	v_pk_add_f32 v[44:45], v[124:125], v[44:45] neg_lo:[0,1] neg_hi:[0,1]
	v_cvt_pk_bf16_f32 v42, v42, v43
	v_cvt_pk_bf16_f32 v43, v44, v45
	ds_write2_b64 v34, v[120:121], v[122:123] offset0:130 offset1:194
	ds_write2_b64 v35, v[40:41], v[42:43] offset0:130 offset1:194
	s_waitcnt lgkmcnt(0)
	s_barrier
	ds_read_b128 v[40:43], v37
	ds_read_b128 v[44:47], v36
	ds_read_b128 v[48:51], v37 offset:64
	ds_read_b128 v[52:55], v36 offset:64
	s_waitcnt lgkmcnt(2)
	v_mfma_f32_16x16x32_bf16 v[6:9], v[40:43], v[44:47], v[6:9]
	ds_read_b128 v[56:59], v38
	ds_read_b128 v[60:63], v38 offset:64
	s_waitcnt lgkmcnt(1)
	v_mfma_f32_16x16x32_bf16 v[6:9], v[56:59], v[44:47], v[6:9]
	ds_read_b128 v[44:47], v36 offset:33280
	ds_read_b128 v[108:111], v36 offset:33344
	s_waitcnt lgkmcnt(1)
	v_mfma_f32_16x16x32_bf16 v[6:9], v[40:43], v[44:47], v[6:9]
	ds_read_b128 v[44:47], v36 offset:16640
	ds_read_b128 v[112:115], v36 offset:16704
	s_waitcnt lgkmcnt(1)
	v_mfma_f32_16x16x32_bf16 v[2:5], v[40:43], v[44:47], v[2:5]
	v_mfma_f32_16x16x32_bf16 v[2:5], v[56:59], v[44:47], v[2:5]
	ds_read_b128 v[44:47], v36 offset:49920
	ds_read_b128 v[56:59], v36 offset:49984
	s_waitcnt lgkmcnt(0)
	s_barrier
	v_mfma_f32_16x16x32_bf16 v[2:5], v[40:43], v[44:47], v[2:5]
	v_mfma_f32_16x16x32_bf16 v[6:9], v[48:51], v[52:55], v[6:9]
	v_mfma_f32_16x16x32_bf16 v[2:5], v[48:51], v[112:115], v[2:5]
	v_mfma_f32_16x16x32_bf16 v[6:9], v[60:63], v[52:55], v[6:9]
	v_mfma_f32_16x16x32_bf16 v[2:5], v[60:63], v[112:115], v[2:5]
	v_mfma_f32_16x16x32_bf16 v[6:9], v[48:51], v[108:111], v[6:9]
	v_mfma_f32_16x16x32_bf16 v[2:5], v[48:51], v[56:59], v[2:5]
	s_and_saveexec_b64 s[54:55], s[4:5]
	s_cbranch_execz .LBB0_934
	v_mov_b32_e32 v39, v151
	v_mov_b32_e32 v40, v70
	v_ashrrev_i32_e32 v46, 3, v40
	v_lshlrev_b32_e32 v42, 1, v46
	v_ashrrev_i32_e32 v43, 31, v42
	v_and_b32_e32 v47, 28, v39
	v_lshlrev_b64 v[42:43], 7, v[42:43]
	v_lshlrev_b32_e32 v72, 2, v47
	v_lshl_add_u64 v[42:43], s[44:45], 0, v[42:43]
	v_lshl_add_u64 v[44:45], v[42:43], 0, v[72:73]
	v_lshlrev_b32_e32 v46, 2, v46
	v_mul_u32_u24_e32 v47, 0x410, v47
	v_add3_u32 v41, 0, v46, v47
	v_add_co_u32_e32 v42, vcc, 0x20000, v44
	s_nop 1
	v_addc_co_u32_e32 v43, vcc, 0, v45, vcc
	global_load_dwordx4 v[216:219], v[42:43], off
	global_load_dwordx4 v[220:223], v[42:43], off offset:128
	v_add_co_u32_e32 v42, vcc, 0x24000, v44
	s_nop 1
	v_addc_co_u32_e32 v43, vcc, 0, v45, vcc
	global_load_dwordx4 v[224:227], v[42:43], off
	global_load_dwordx4 v[228:231], v[42:43], off offset:128
	v_add_co_u32_e32 v42, vcc, 0x28000, v44
	s_nop 1
	v_addc_co_u32_e32 v43, vcc, 0, v45, vcc
	global_load_dwordx4 v[232:235], v[42:43], off
	global_load_dwordx4 v[236:239], v[42:43], off offset:128
	v_add_co_u32_e32 v42, vcc, 0x2c000, v44
	s_nop 1
	v_addc_co_u32_e32 v43, vcc, 0, v45, vcc
	global_load_dwordx4 v[240:243], v[42:43], off
	global_load_dwordx4 v[248:251], v[42:43], off offset:128
	s_waitcnt vmcnt(0)
; #define LAS __attribute__((address_space(3)))
; __device__ __forceinline__ unsigned cvtpk(float lo, float hi) { f32x2_t v = {lo, hi}; bf16x2_t b = __builtin_convertvector(v, bf16x2_t); return __builtin_bit_cast(unsigned, b); }
; __device__ __forceinline__ float bflo(unsigned w) { return __uint_as_float(w << 16); }
; __device__ __forceinline__ float bfhi(unsigned w) { return __uint_as_float(w & 0xffff0000u); }
; __device__ __forceinline__ void phase_norm2_route(const Ptrs& p, LAS unsigned char* lds) {
;     ...
;                 for (int i = tid; i < 2048; i += 512) { const int kp = i >> 3, cq = i & 7; const float* w = p.router_w + (size_t)(512 * ch + 2 * kp) * E + cq * 4;
;                     const f32x4 w0 = *(const f32x4*)w, w1 = *(const f32x4*)(w + E);
; #pragma unroll
;                     for (int j = 0; j < 4; ++j) { const unsigned hi = cvtpk(w0[j], w1[j]), lo = cvtpk(w0[j] - bflo(hi), w1[j] - bfhi(hi));
;                         *(LAS unsigned*)(lds + R_WHI + (cq * 4 + j) * R_PITCH + kp * 4) = hi; *(LAS unsigned*)(lds + R_WLO + (cq * 4 + j) * R_PITCH + kp * 4) = lo; } }
	v_cvt_pk_bf16_f32 v48, v216, v220
	v_cvt_pk_bf16_f32 v49, v217, v221
	v_cvt_pk_bf16_f32 v50, v218, v222
	v_cvt_pk_bf16_f32 v51, v219, v223
	ds_write_b32 v41, v48
	ds_write_b32 v41, v49 offset:1040
	ds_write_b32 v41, v50 offset:2080
	ds_write_b32 v41, v51 offset:3120
	v_lshlrev_b32_e32 v46, 16, v48
	v_and_b32_e32 v47, 0xffff0000, v48
	v_sub_f32_e32 v46, v216, v46
	v_sub_f32_e32 v47, v220, v47
	v_cvt_pk_bf16_f32 v48, v46, v47
	v_lshlrev_b32_e32 v46, 16, v49
	v_and_b32_e32 v47, 0xffff0000, v49
	v_sub_f32_e32 v46, v217, v46
	v_sub_f32_e32 v47, v221, v47
	v_cvt_pk_bf16_f32 v49, v46, v47
	v_lshlrev_b32_e32 v46, 16, v50
	v_and_b32_e32 v47, 0xffff0000, v50
	v_sub_f32_e32 v46, v218, v46
	v_sub_f32_e32 v47, v222, v47
	v_cvt_pk_bf16_f32 v50, v46, v47
	v_lshlrev_b32_e32 v46, 16, v51
	v_and_b32_e32 v47, 0xffff0000, v51
	v_sub_f32_e32 v46, v219, v46
	v_sub_f32_e32 v47, v223, v47
	v_cvt_pk_bf16_f32 v51, v46, v47
	ds_write_b32 v41, v48 offset:33280
	ds_write_b32 v41, v49 offset:34320
	ds_write_b32 v41, v50 offset:35360
	ds_write_b32 v41, v51 offset:36400
	v_cvt_pk_bf16_f32 v48, v224, v228
	v_cvt_pk_bf16_f32 v49, v225, v229
	v_cvt_pk_bf16_f32 v50, v226, v230
	v_cvt_pk_bf16_f32 v51, v227, v231
	ds_write_b32 v41, v48 offset:256
	ds_write_b32 v41, v49 offset:1296
	ds_write_b32 v41, v50 offset:2336
	ds_write_b32 v41, v51 offset:3376
	v_lshlrev_b32_e32 v46, 16, v48
	v_and_b32_e32 v47, 0xffff0000, v48
	v_sub_f32_e32 v46, v224, v46
	v_sub_f32_e32 v47, v228, v47
	v_cvt_pk_bf16_f32 v48, v46, v47
	v_lshlrev_b32_e32 v46, 16, v49
	v_and_b32_e32 v47, 0xffff0000, v49
	v_sub_f32_e32 v46, v225, v46
	v_sub_f32_e32 v47, v229, v47
	v_cvt_pk_bf16_f32 v49, v46, v47
	v_lshlrev_b32_e32 v46, 16, v50
	v_and_b32_e32 v47, 0xffff0000, v50
	v_sub_f32_e32 v46, v226, v46
	v_sub_f32_e32 v47, v230, v47
	v_cvt_pk_bf16_f32 v50, v46, v47
	v_lshlrev_b32_e32 v46, 16, v51
	v_and_b32_e32 v47, 0xffff0000, v51
	v_sub_f32_e32 v46, v227, v46
	v_sub_f32_e32 v47, v231, v47
	v_cvt_pk_bf16_f32 v51, v46, v47
	ds_write_b32 v41, v48 offset:33536
	ds_write_b32 v41, v49 offset:34576
	ds_write_b32 v41, v50 offset:35616
	ds_write_b32 v41, v51 offset:36656
	v_cvt_pk_bf16_f32 v48, v232, v236
	v_cvt_pk_bf16_f32 v49, v233, v237
	v_cvt_pk_bf16_f32 v50, v234, v238
	v_cvt_pk_bf16_f32 v51, v235, v239
	ds_write_b32 v41, v48 offset:512
	ds_write_b32 v41, v49 offset:1552
	ds_write_b32 v41, v50 offset:2592
	ds_write_b32 v41, v51 offset:3632
	v_lshlrev_b32_e32 v46, 16, v48
	v_and_b32_e32 v47, 0xffff0000, v48
	v_sub_f32_e32 v46, v232, v46
	v_sub_f32_e32 v47, v236, v47
	v_cvt_pk_bf16_f32 v48, v46, v47
	v_lshlrev_b32_e32 v46, 16, v49
	v_and_b32_e32 v47, 0xffff0000, v49
	v_sub_f32_e32 v46, v233, v46
	v_sub_f32_e32 v47, v237, v47
	v_cvt_pk_bf16_f32 v49, v46, v47
	v_lshlrev_b32_e32 v46, 16, v50
	v_and_b32_e32 v47, 0xffff0000, v50
	v_sub_f32_e32 v46, v234, v46
	v_sub_f32_e32 v47, v238, v47
	v_cvt_pk_bf16_f32 v50, v46, v47
	v_lshlrev_b32_e32 v46, 16, v51
	v_and_b32_e32 v47, 0xffff0000, v51
	v_sub_f32_e32 v46, v235, v46
	v_sub_f32_e32 v47, v239, v47
	v_cvt_pk_bf16_f32 v51, v46, v47
	ds_write_b32 v41, v48 offset:33792
	ds_write_b32 v41, v49 offset:34832
	ds_write_b32 v41, v50 offset:35872
	ds_write_b32 v41, v51 offset:36912
	v_cvt_pk_bf16_f32 v48, v240, v248
	v_cvt_pk_bf16_f32 v49, v241, v249
	v_cvt_pk_bf16_f32 v50, v242, v250
	v_cvt_pk_bf16_f32 v51, v243, v251
	ds_write_b32 v41, v48 offset:768
	ds_write_b32 v41, v49 offset:1808
	ds_write_b32 v41, v50 offset:2848
	ds_write_b32 v41, v51 offset:3888
	v_lshlrev_b32_e32 v46, 16, v48
	v_and_b32_e32 v47, 0xffff0000, v48
	v_sub_f32_e32 v46, v240, v46
	v_sub_f32_e32 v47, v248, v47
	v_cvt_pk_bf16_f32 v48, v46, v47
	v_lshlrev_b32_e32 v46, 16, v49
	v_and_b32_e32 v47, 0xffff0000, v49
	v_sub_f32_e32 v46, v241, v46
	v_sub_f32_e32 v47, v249, v47
	v_cvt_pk_bf16_f32 v49, v46, v47
	v_lshlrev_b32_e32 v46, 16, v50
	v_and_b32_e32 v47, 0xffff0000, v50
	v_sub_f32_e32 v46, v242, v46
	v_sub_f32_e32 v47, v250, v47
	v_cvt_pk_bf16_f32 v50, v46, v47
	v_lshlrev_b32_e32 v46, 16, v51
	v_and_b32_e32 v47, 0xffff0000, v51
	v_sub_f32_e32 v46, v243, v46
	v_sub_f32_e32 v47, v251, v47
	v_cvt_pk_bf16_f32 v51, v46, v47
	ds_write_b32 v41, v48 offset:34048
	ds_write_b32 v41, v49 offset:35088
	ds_write_b32 v41, v50 offset:36128
	ds_write_b32 v41, v51 offset:37168
; #define LAS __attribute__((address_space(3)))
; __device__ __forceinline__ unsigned cvtpk(float lo, float hi) { f32x2_t v = {lo, hi}; bf16x2_t b = __builtin_convertvector(v, bf16x2_t); return __builtin_bit_cast(unsigned, b); }
; __device__ __forceinline__ float bflo(unsigned w) { return __uint_as_float(w << 16); }
; __device__ __forceinline__ float bfhi(unsigned w) { return __uint_as_float(w & 0xffff0000u); }
; __device__ __forceinline__ void phase_norm2_route(const Ptrs& p, LAS unsigned char* lds) {
;     ...
;                 for (int q = 0; q < 2; ++q)
; #pragma unroll
;                     for (int cc = 0; cc < 2; ++cc) { const f32x4 h4 = v[q][2 * ch + cc]; u32x2 hi, lo; hi.x = cvtpk(h4[0], h4[1]); hi.y = cvtpk(h4[2], h4[3]);
;                         lo.x = cvtpk(h4[0] - bflo(hi.x), h4[1] - bfhi(hi.x)); lo.y = cvtpk(h4[2] - bflo(hi.y), h4[3] - bfhi(hi.y));
;                         const int o = (wid * 2 + q) * R_PITCH + (cc * 256 + lane * 4) * 2;
;                         *(LAS u32x2*)(lds + R_HHI + o) = hi; *(LAS u32x2*)(lds + R_HLO + o) = lo; }
;                 __syncthreads();
; #pragma unroll
;                 for (int s2 = 0; s2 < 2; ++s2) { const int off = (lane & 15) * R_PITCH + (2 * wid + s2) * 64 + (lane >> 4) * 16;
;                     const bf16x8 ahi = *(const LAS bf16x8*)(lds + R_HHI + off), alo = *(const LAS bf16x8*)(lds + R_HLO + off);
; #pragma unroll
;                     for (int ct = 0; ct < 2; ++ct) { const bf16x8 bhi = *(const LAS bf16x8*)(lds + R_WHI + ct * 16 * R_PITCH + off), blo = *(const LAS bf16x8*)(lds + R_WLO + ct * 16 * R_PITCH + off);
;                         acc[ct] = __builtin_amdgcn_mfma_f32_16x16x32_bf16(ahi, bhi, acc[ct], 0, 0, 0); acc[ct] = __builtin_amdgcn_mfma_f32_16x16x32_bf16(alo, bhi, acc[ct], 0, 0, 0);
;                         acc[ct] = __builtin_amdgcn_mfma_f32_16x16x32_bf16(ahi, blo, acc[ct], 0, 0, 0); } }
.LBB0_934:
	s_or_b64 exec, exec, s[54:55]
	v_lshlrev_b32_e32 v40, 16, v96
	v_and_b32_e32 v41, 0xffff0000, v96
	v_lshlrev_b32_e32 v42, 16, v97
	v_and_b32_e32 v43, 0xffff0000, v97
	v_pk_add_f32 v[40:41], v[100:101], v[40:41] neg_lo:[0,1] neg_hi:[0,1]
	v_pk_add_f32 v[42:43], v[98:99], v[42:43] neg_lo:[0,1] neg_hi:[0,1]
	v_cvt_pk_bf16_f32 v40, v40, v41
	v_cvt_pk_bf16_f32 v41, v42, v43
	v_lshlrev_b32_e32 v42, 16, v102
	v_and_b32_e32 v43, 0xffff0000, v102
	v_lshlrev_b32_e32 v44, 16, v103
	v_and_b32_e32 v45, 0xffff0000, v103
	v_pk_add_f32 v[42:43], v[106:107], v[42:43] neg_lo:[0,1] neg_hi:[0,1]
	v_pk_add_f32 v[44:45], v[104:105], v[44:45] neg_lo:[0,1] neg_hi:[0,1]
	v_cvt_pk_bf16_f32 v42, v42, v43
	v_cvt_pk_bf16_f32 v43, v44, v45
	ds_write2st64_b64 v34, v[96:97], v[102:103] offset1:1
	ds_write2st64_b64 v35, v[40:41], v[42:43] offset1:1
	v_lshlrev_b32_e32 v40, 16, v22
	v_and_b32_e32 v41, 0xffff0000, v22
	v_pk_add_f32 v[32:33], v[32:33], v[40:41] neg_lo:[0,1] neg_hi:[0,1]
	v_lshlrev_b32_e32 v40, 16, v23
	v_and_b32_e32 v41, 0xffff0000, v23
	v_pk_add_f32 v[28:29], v[28:29], v[40:41] neg_lo:[0,1] neg_hi:[0,1]
	v_cvt_pk_bf16_f32 v32, v32, v33
	v_cvt_pk_bf16_f32 v33, v28, v29
	v_lshlrev_b32_e32 v28, 16, v24
	v_and_b32_e32 v29, 0xffff0000, v24
	v_pk_add_f32 v[28:29], v[30:31], v[28:29] neg_lo:[0,1] neg_hi:[0,1]
	v_lshlrev_b32_e32 v30, 16, v25
	v_and_b32_e32 v31, 0xffff0000, v25
	v_pk_add_f32 v[26:27], v[26:27], v[30:31] neg_lo:[0,1] neg_hi:[0,1]
	v_cvt_pk_bf16_f32 v28, v28, v29
	v_cvt_pk_bf16_f32 v29, v26, v27
	ds_write2_b64 v34, v[22:23], v[24:25] offset0:130 offset1:194
	ds_write2_b64 v35, v[32:33], v[28:29] offset0:130 offset1:194
	s_waitcnt lgkmcnt(0)
	s_barrier
	ds_read_b128 v[22:25], v37
	ds_read_b128 v[26:29], v36
	ds_read_b128 v[30:33], v37 offset:64
	ds_read_b128 v[40:43], v36 offset:64
	s_waitcnt lgkmcnt(2)
	v_mfma_f32_16x16x32_bf16 v[6:9], v[22:25], v[26:29], v[6:9]
	ds_read_b128 v[44:47], v38
	ds_read_b128 v[48:51], v38 offset:64
	s_waitcnt lgkmcnt(1)
	v_mfma_f32_16x16x32_bf16 v[6:9], v[44:47], v[26:29], v[6:9]
	ds_read_b128 v[26:29], v36 offset:33280
	ds_read_b128 v[52:55], v36 offset:33344
	s_waitcnt lgkmcnt(1)
	v_mfma_f32_16x16x32_bf16 v[6:9], v[22:25], v[26:29], v[6:9]
	ds_read_b128 v[26:29], v36 offset:16640
	ds_read_b128 v[56:59], v36 offset:16704
	s_waitcnt lgkmcnt(1)
	v_mfma_f32_16x16x32_bf16 v[2:5], v[22:25], v[26:29], v[2:5]
	v_mfma_f32_16x16x32_bf16 v[2:5], v[44:47], v[26:29], v[2:5]
	ds_read_b128 v[26:29], v36 offset:49920
	ds_read_b128 v[44:47], v36 offset:49984
	s_waitcnt lgkmcnt(0)
	s_barrier
	v_mfma_f32_16x16x32_bf16 v[2:5], v[22:25], v[26:29], v[2:5]
	v_mfma_f32_16x16x32_bf16 v[6:9], v[30:33], v[40:43], v[6:9]
	v_mfma_f32_16x16x32_bf16 v[2:5], v[30:33], v[56:59], v[2:5]
	v_mfma_f32_16x16x32_bf16 v[6:9], v[48:51], v[40:43], v[6:9]
	v_mfma_f32_16x16x32_bf16 v[2:5], v[48:51], v[56:59], v[2:5]
	v_mfma_f32_16x16x32_bf16 v[6:9], v[30:33], v[52:55], v[6:9]
	v_mfma_f32_16x16x32_bf16 v[2:5], v[30:33], v[44:47], v[2:5]
	s_and_saveexec_b64 s[54:55], s[4:5]
	s_cbranch_execz .LBB0_924
; #define LAS __attribute__((address_space(3)))
; __device__ __forceinline__ unsigned cvtpk(float lo, float hi) { f32x2_t v = {lo, hi}; bf16x2_t b = __builtin_convertvector(v, bf16x2_t); return __builtin_bit_cast(unsigned, b); }
; __device__ __forceinline__ float bflo(unsigned w) { return __uint_as_float(w << 16); }
; __device__ __forceinline__ float bfhi(unsigned w) { return __uint_as_float(w & 0xffff0000u); }
; __device__ __forceinline__ void phase_norm2_route(const Ptrs& p, LAS unsigned char* lds) {
;     ...
;                 for (int i = tid; i < 2048; i += 512) { const int kp = i >> 3, cq = i & 7; const float* w = p.router_w + (size_t)(512 * ch + 2 * kp) * E + cq * 4;
;                     const f32x4 w0 = *(const f32x4*)w, w1 = *(const f32x4*)(w + E);
; #pragma unroll
;                     for (int j = 0; j < 4; ++j) { const unsigned hi = cvtpk(w0[j], w1[j]), lo = cvtpk(w0[j] - bflo(hi), w1[j] - bfhi(hi));
;                         *(LAS unsigned*)(lds + R_WHI + (cq * 4 + j) * R_PITCH + kp * 4) = hi; *(LAS unsigned*)(lds + R_WLO + (cq * 4 + j) * R_PITCH + kp * 4) = lo; } }
	v_mov_b32_e32 v22, v151
	v_mov_b32_e32 v23, v70
	v_ashrrev_i32_e32 v29, 3, v23
	v_lshlrev_b32_e32 v24, 1, v29
	v_ashrrev_i32_e32 v25, 31, v24
	v_and_b32_e32 v30, 28, v22
	v_lshlrev_b64 v[24:25], 7, v[24:25]
	v_lshlrev_b32_e32 v72, 2, v30
	v_lshl_add_u64 v[24:25], s[44:45], 0, v[24:25]
	v_lshl_add_u64 v[26:27], v[24:25], 0, v[72:73]
	v_lshlrev_b32_e32 v29, 2, v29
	v_mul_u32_u24_e32 v30, 0x410, v30
	v_add3_u32 v28, 0, v29, v30
	v_add_co_u32_e32 v24, vcc, 0x30000, v26
	s_nop 1
	v_addc_co_u32_e32 v25, vcc, 0, v27, vcc
	global_load_dwordx4 v[216:219], v[24:25], off
	global_load_dwordx4 v[220:223], v[24:25], off offset:128
	v_add_co_u32_e32 v24, vcc, 0x34000, v26
	s_nop 1
	v_addc_co_u32_e32 v25, vcc, 0, v27, vcc
	global_load_dwordx4 v[224:227], v[24:25], off
	global_load_dwordx4 v[228:231], v[24:25], off offset:128
	v_add_co_u32_e32 v24, vcc, 0x38000, v26
	s_nop 1
	v_addc_co_u32_e32 v25, vcc, 0, v27, vcc
	global_load_dwordx4 v[232:235], v[24:25], off
	global_load_dwordx4 v[236:239], v[24:25], off offset:128
	v_add_co_u32_e32 v24, vcc, 0x3c000, v26
	s_nop 1
	v_addc_co_u32_e32 v25, vcc, 0, v27, vcc
	global_load_dwordx4 v[240:243], v[24:25], off
	global_load_dwordx4 v[248:251], v[24:25], off offset:128
	s_waitcnt vmcnt(0)
	v_cvt_pk_bf16_f32 v31, v216, v220
	v_cvt_pk_bf16_f32 v32, v217, v221
	v_cvt_pk_bf16_f32 v33, v218, v222
	v_cvt_pk_bf16_f32 v39, v219, v223
	ds_write_b32 v28, v31
	ds_write_b32 v28, v32 offset:1040
	ds_write_b32 v28, v33 offset:2080
	ds_write_b32 v28, v39 offset:3120
	v_lshlrev_b32_e32 v29, 16, v31
	v_and_b32_e32 v30, 0xffff0000, v31
	v_sub_f32_e32 v29, v216, v29
	v_sub_f32_e32 v30, v220, v30
	v_cvt_pk_bf16_f32 v31, v29, v30
	v_lshlrev_b32_e32 v29, 16, v32
	v_and_b32_e32 v30, 0xffff0000, v32
	v_sub_f32_e32 v29, v217, v29
	v_sub_f32_e32 v30, v221, v30
	v_cvt_pk_bf16_f32 v32, v29, v30
	v_lshlrev_b32_e32 v29, 16, v33
	v_and_b32_e32 v30, 0xffff0000, v33
	v_sub_f32_e32 v29, v218, v29
	v_sub_f32_e32 v30, v222, v30
	v_cvt_pk_bf16_f32 v33, v29, v30
	v_lshlrev_b32_e32 v29, 16, v39
	v_and_b32_e32 v30, 0xffff0000, v39
	v_sub_f32_e32 v29, v219, v29
	v_sub_f32_e32 v30, v223, v30
	v_cvt_pk_bf16_f32 v39, v29, v30
	ds_write_b32 v28, v31 offset:33280
	ds_write_b32 v28, v32 offset:34320
	ds_write_b32 v28, v33 offset:35360
	ds_write_b32 v28, v39 offset:36400
	v_cvt_pk_bf16_f32 v31, v224, v228
	v_cvt_pk_bf16_f32 v32, v225, v229
	v_cvt_pk_bf16_f32 v33, v226, v230
	v_cvt_pk_bf16_f32 v39, v227, v231
	ds_write_b32 v28, v31 offset:256
	ds_write_b32 v28, v32 offset:1296
	ds_write_b32 v28, v33 offset:2336
	ds_write_b32 v28, v39 offset:3376
	v_lshlrev_b32_e32 v29, 16, v31
	v_and_b32_e32 v30, 0xffff0000, v31
	v_sub_f32_e32 v29, v224, v29
	v_sub_f32_e32 v30, v228, v30
	v_cvt_pk_bf16_f32 v31, v29, v30
	v_lshlrev_b32_e32 v29, 16, v32
	v_and_b32_e32 v30, 0xffff0000, v32
	v_sub_f32_e32 v29, v225, v29
	v_sub_f32_e32 v30, v229, v30
	v_cvt_pk_bf16_f32 v32, v29, v30
	v_lshlrev_b32_e32 v29, 16, v33
	v_and_b32_e32 v30, 0xffff0000, v33
	v_sub_f32_e32 v29, v226, v29
	v_sub_f32_e32 v30, v230, v30
	v_cvt_pk_bf16_f32 v33, v29, v30
	v_lshlrev_b32_e32 v29, 16, v39
	v_and_b32_e32 v30, 0xffff0000, v39
	v_sub_f32_e32 v29, v227, v29
	v_sub_f32_e32 v30, v231, v30
	v_cvt_pk_bf16_f32 v39, v29, v30
	ds_write_b32 v28, v31 offset:33536
	ds_write_b32 v28, v32 offset:34576
	ds_write_b32 v28, v33 offset:35616
	ds_write_b32 v28, v39 offset:36656
	v_cvt_pk_bf16_f32 v31, v232, v236
	v_cvt_pk_bf16_f32 v32, v233, v237
	v_cvt_pk_bf16_f32 v33, v234, v238
	v_cvt_pk_bf16_f32 v39, v235, v239
	ds_write_b32 v28, v31 offset:512
	ds_write_b32 v28, v32 offset:1552
	ds_write_b32 v28, v33 offset:2592
	ds_write_b32 v28, v39 offset:3632
	v_lshlrev_b32_e32 v29, 16, v31
	v_and_b32_e32 v30, 0xffff0000, v31
	v_sub_f32_e32 v29, v232, v29
	v_sub_f32_e32 v30, v236, v30
	v_cvt_pk_bf16_f32 v31, v29, v30
	v_lshlrev_b32_e32 v29, 16, v32
	v_and_b32_e32 v30, 0xffff0000, v32
	v_sub_f32_e32 v29, v233, v29
	v_sub_f32_e32 v30, v237, v30
	v_cvt_pk_bf16_f32 v32, v29, v30
	v_lshlrev_b32_e32 v29, 16, v33
	v_and_b32_e32 v30, 0xffff0000, v33
	v_sub_f32_e32 v29, v234, v29
	v_sub_f32_e32 v30, v238, v30
	v_cvt_pk_bf16_f32 v33, v29, v30
	v_lshlrev_b32_e32 v29, 16, v39
	v_and_b32_e32 v30, 0xffff0000, v39
	v_sub_f32_e32 v29, v235, v29
	v_sub_f32_e32 v30, v239, v30
	v_cvt_pk_bf16_f32 v39, v29, v30
	ds_write_b32 v28, v31 offset:33792
	ds_write_b32 v28, v32 offset:34832
	ds_write_b32 v28, v33 offset:35872
	ds_write_b32 v28, v39 offset:36912
	v_cvt_pk_bf16_f32 v31, v240, v248
	v_cvt_pk_bf16_f32 v32, v241, v249
	v_cvt_pk_bf16_f32 v33, v242, v250
	v_cvt_pk_bf16_f32 v39, v243, v251
	ds_write_b32 v28, v31 offset:768
	ds_write_b32 v28, v32 offset:1808
	ds_write_b32 v28, v33 offset:2848
	ds_write_b32 v28, v39 offset:3888
	v_lshlrev_b32_e32 v29, 16, v31
	v_and_b32_e32 v30, 0xffff0000, v31
	v_sub_f32_e32 v29, v240, v29
	v_sub_f32_e32 v30, v248, v30
	v_cvt_pk_bf16_f32 v31, v29, v30
	v_lshlrev_b32_e32 v29, 16, v32
	v_and_b32_e32 v30, 0xffff0000, v32
	v_sub_f32_e32 v29, v241, v29
	v_sub_f32_e32 v30, v249, v30
	v_cvt_pk_bf16_f32 v32, v29, v30
	v_lshlrev_b32_e32 v29, 16, v33
	v_and_b32_e32 v30, 0xffff0000, v33
	v_sub_f32_e32 v29, v242, v29
	v_sub_f32_e32 v30, v250, v30
	v_cvt_pk_bf16_f32 v33, v29, v30
	v_lshlrev_b32_e32 v29, 16, v39
	v_and_b32_e32 v30, 0xffff0000, v39
	v_sub_f32_e32 v29, v243, v29
	v_sub_f32_e32 v30, v251, v30
	v_cvt_pk_bf16_f32 v39, v29, v30
	ds_write_b32 v28, v31 offset:34048
	ds_write_b32 v28, v32 offset:35088
	ds_write_b32 v28, v33 offset:36128
	ds_write_b32 v28, v39 offset:37168
	s_branch .LBB0_924
